# P2 CAT stores (attention epilogue and pooling) with sc1 (write-through)
# speedup vs baseline: 1.0133x; 1.0051x over previous
.LBB0_287:
	s_or_b64 exec, exec, s[4:5]
	s_waitcnt lgkmcnt(0)
	ds_read_b128 v[66:69], v179
	ds_read_b128 v[74:77], v179 offset:32
	ds_read_b128 v[82:85], v179 offset:64
	ds_read_b128 v[86:89], v179 offset:96
	s_lshl_b32 s0, s76, 13
	s_waitcnt lgkmcnt(3)
	v_rcp_f32_e32 v78, v66
	v_rcp_f32_e32 v79, v67
	v_rcp_f32_e32 v72, v68
	v_rcp_f32_e32 v73, v69
	s_waitcnt lgkmcnt(2)
	v_rcp_f32_e32 v68, v74
	v_rcp_f32_e32 v80, v75
	v_rcp_f32_e32 v74, v76
	v_rcp_f32_e32 v75, v77
	s_waitcnt lgkmcnt(1)
	v_rcp_f32_e32 v81, v82
	v_rcp_f32_e32 v82, v83
	v_rcp_f32_e32 v76, v84
	v_rcp_f32_e32 v77, v85
	s_waitcnt lgkmcnt(0)
	v_rcp_f32_e32 v69, v86
	v_rcp_f32_e32 v70, v87
	v_rcp_f32_e32 v66, v88
	v_rcp_f32_e32 v67, v89
	s_add_i32 s0, s0, 0
	s_add_i32 s0, s0, 0x14800
	s_cmp_lg_u32 s97, 1
	v_lshl_add_u32 v71, v163, 2, s0
	s_mov_b64 s[4:5], -1
	s_cbranch_scc0 .LBB0_289
	ds_read2st64_b32 v[84:85], v71 offset1:1
	ds_read2st64_b32 v[86:87], v71 offset0:2 offset1:3
	ds_read2st64_b32 v[88:89], v71 offset0:4 offset1:5
	ds_read2st64_b32 v[96:97], v71 offset0:6 offset1:7
	v_readlane_b32 s4, v254, 9
	s_waitcnt lgkmcnt(3)
	v_lshlrev_b32_e32 v83, 16, v84
	v_and_b32_e32 v84, 0xffff0000, v84
	v_mul_f32_e32 v83, v157, v83
	v_fma_f32 v138, v18, v78, -v83
	v_mul_f32_e32 v83, v157, v84
	v_fma_f32 v134, v19, v79, -v83
	v_lshlrev_b32_e32 v83, 16, v85
	v_mul_f32_e32 v83, v157, v83
	v_fma_f32 v130, v20, v72, -v83
	v_and_b32_e32 v83, 0xffff0000, v85
	v_mul_f32_e32 v83, v157, v83
	v_fma_f32 v125, v21, v73, -v83
	s_waitcnt lgkmcnt(2)
	v_lshlrev_b32_e32 v83, 16, v86
	v_mul_f32_e32 v83, v157, v83
	v_fma_f32 v121, v22, v68, -v83
	v_and_b32_e32 v83, 0xffff0000, v86
	v_mul_f32_e32 v83, v157, v83
	v_fma_f32 v101, v23, v80, -v83
	v_lshlrev_b32_e32 v83, 16, v87
	v_mul_f32_e32 v83, v157, v83
	v_fma_f32 v98, v24, v74, -v83
	v_and_b32_e32 v83, 0xffff0000, v87
	v_mul_f32_e32 v83, v157, v83
	v_fma_f32 v95, v25, v75, -v83
	s_waitcnt lgkmcnt(1)
	v_lshlrev_b32_e32 v83, 16, v88
	v_mul_f32_e32 v83, v157, v83
	v_fma_f32 v92, v26, v81, -v83
	v_and_b32_e32 v83, 0xffff0000, v88
	v_mul_f32_e32 v83, v157, v83
	v_fma_f32 v90, v27, v82, -v83
	v_lshlrev_b32_e32 v83, 16, v89
	v_mul_f32_e32 v83, v157, v83
	v_fma_f32 v88, v28, v76, -v83
	v_and_b32_e32 v83, 0xffff0000, v89
	v_mul_f32_e32 v83, v157, v83
	v_fma_f32 v87, v29, v77, -v83
	s_waitcnt lgkmcnt(0)
	v_lshlrev_b32_e32 v83, 16, v96
	v_mul_f32_e32 v83, v157, v83
	v_fma_f32 v86, v30, v69, -v83
	v_and_b32_e32 v83, 0xffff0000, v96
	v_mul_f32_e32 v83, v157, v83
	v_fma_f32 v85, v31, v70, -v83
	v_lshlrev_b32_e32 v83, 16, v97
	v_mul_f32_e32 v83, v157, v83
	v_fma_f32 v84, v32, v66, -v83
	v_and_b32_e32 v83, 0xffff0000, v97
	ds_read2st64_b32 v[96:97], v71 offset0:8 offset1:9
	ds_read2st64_b32 v[122:123], v71 offset0:10 offset1:11
	ds_read2st64_b32 v[128:129], v71 offset0:12 offset1:13
	ds_read2st64_b32 v[142:143], v71 offset0:14 offset1:15
	v_mul_f32_e32 v83, v157, v83
	v_fma_f32 v83, v33, v67, -v83
	v_readlane_b32 s5, v254, 10
	s_waitcnt lgkmcnt(3)
	v_lshlrev_b32_e32 v89, 16, v96
	v_mul_f32_e32 v89, v157, v89
	v_fma_f32 v150, v34, v78, -v89
	v_and_b32_e32 v89, 0xffff0000, v96
	v_mul_f32_e32 v89, v157, v89
	v_fma_f32 v147, v35, v79, -v89
	v_lshlrev_b32_e32 v89, 16, v97
	v_mul_f32_e32 v89, v157, v89
	v_fma_f32 v144, v36, v72, -v89
	v_and_b32_e32 v89, 0xffff0000, v97
	v_mul_f32_e32 v89, v157, v89
	v_fma_f32 v141, v37, v73, -v89
	s_waitcnt lgkmcnt(2)
	v_lshlrev_b32_e32 v89, 16, v122
	v_mul_f32_e32 v89, v157, v89
	v_fma_f32 v136, v38, v68, -v89
	v_and_b32_e32 v89, 0xffff0000, v122
	v_mul_f32_e32 v89, v157, v89
	v_fma_f32 v132, v39, v80, -v89
	v_lshlrev_b32_e32 v89, 16, v123
	v_mul_f32_e32 v89, v157, v89
	v_fma_f32 v127, v40, v74, -v89
	v_and_b32_e32 v89, 0xffff0000, v123
	v_mul_f32_e32 v89, v157, v89
	v_fma_f32 v123, v41, v75, -v89
	s_waitcnt lgkmcnt(1)
	v_lshlrev_b32_e32 v89, 16, v128
	v_mul_f32_e32 v89, v157, v89
	v_fma_f32 v120, v42, v81, -v89
	v_and_b32_e32 v89, 0xffff0000, v128
	v_mul_f32_e32 v89, v157, v89
	v_fma_f32 v100, v43, v82, -v89
	v_lshlrev_b32_e32 v89, 16, v129
	v_mul_f32_e32 v89, v157, v89
	v_fma_f32 v97, v44, v76, -v89
	v_and_b32_e32 v89, 0xffff0000, v129
	ds_read2st64_b32 v[128:129], v71 offset0:16 offset1:17
	v_mul_f32_e32 v89, v157, v89
	v_fma_f32 v94, v45, v77, -v89
	s_waitcnt lgkmcnt(1)
	v_lshlrev_b32_e32 v89, 16, v142
	v_mul_f32_e32 v89, v157, v89
	s_waitcnt lgkmcnt(0)
	v_lshlrev_b32_e32 v99, 16, v128
	v_fma_f32 v96, v46, v69, -v89
	v_and_b32_e32 v89, 0xffff0000, v142
	v_mul_f32_e32 v99, v157, v99
	v_mul_f32_e32 v89, v157, v89
	v_fma_f32 v171, v50, v78, -v99
	v_and_b32_e32 v99, 0xffff0000, v128
	v_fma_f32 v93, v47, v70, -v89
	v_lshlrev_b32_e32 v89, 16, v143
	v_mul_f32_e32 v99, v157, v99
	v_mul_f32_e32 v89, v157, v89
	v_fma_f32 v168, v51, v79, -v99
	v_lshlrev_b32_e32 v99, 16, v129
	v_fma_f32 v91, v48, v66, -v89
	v_and_b32_e32 v89, 0xffff0000, v143
	ds_read2st64_b32 v[142:143], v71 offset0:18 offset1:19
	ds_read2st64_b32 v[198:199], v71 offset0:20 offset1:21
	ds_read2st64_b32 v[200:201], v71 offset0:22 offset1:23
	v_mul_f32_e32 v99, v157, v99
	v_fma_f32 v155, v52, v72, -v99
	v_and_b32_e32 v99, 0xffff0000, v129
	v_mul_f32_e32 v99, v157, v99
	v_fma_f32 v153, v53, v73, -v99
	s_waitcnt lgkmcnt(2)
	v_lshlrev_b32_e32 v99, 16, v142
	v_mul_f32_e32 v99, v157, v99
	v_fma_f32 v151, v54, v68, -v99
	v_and_b32_e32 v99, 0xffff0000, v142
	v_mul_f32_e32 v99, v157, v99
	v_fma_f32 v148, v55, v80, -v99
	v_lshlrev_b32_e32 v99, 16, v143
	v_mul_f32_e32 v99, v157, v99
	v_fma_f32 v145, v56, v74, -v99
	v_and_b32_e32 v99, 0xffff0000, v143
	v_mul_f32_e32 v99, v157, v99
	v_fma_f32 v142, v57, v75, -v99
	s_waitcnt lgkmcnt(1)
	v_lshlrev_b32_e32 v99, 16, v198
	v_mul_f32_e32 v99, v157, v99
	v_fma_f32 v137, v58, v81, -v99
	v_and_b32_e32 v99, 0xffff0000, v198
	v_mul_f32_e32 v99, v157, v99
	v_fma_f32 v133, v59, v82, -v99
	v_lshlrev_b32_e32 v99, 16, v199
	v_mul_f32_e32 v99, v157, v99
	v_fma_f32 v129, v60, v76, -v99
	v_and_b32_e32 v99, 0xffff0000, v199
	ds_read2st64_b32 v[198:199], v71 offset0:24 offset1:25
	v_mul_f32_e32 v99, v157, v99
	v_fma_f32 v124, v61, v77, -v99
	s_waitcnt lgkmcnt(1)
	v_lshlrev_b32_e32 v99, 16, v200
	v_mul_f32_e32 v99, v157, v99
	s_waitcnt lgkmcnt(0)
	v_lshlrev_b32_e32 v128, 16, v198
	v_fma_f32 v126, v62, v69, -v99
	v_and_b32_e32 v99, 0xffff0000, v200
	v_mul_f32_e32 v128, v157, v128
	v_mul_f32_e32 v99, v157, v99
	v_fma_f32 v182, v2, v78, -v128
	v_and_b32_e32 v128, 0xffff0000, v198
	v_fma_f32 v122, v63, v70, -v99
	v_lshlrev_b32_e32 v99, 16, v201
	v_mul_f32_e32 v128, v157, v128
	v_mul_f32_e32 v99, v157, v99
	v_fma_f32 v180, v3, v79, -v128
	v_lshlrev_b32_e32 v128, 16, v199
	v_fma_f32 v118, v64, v66, -v99
	v_and_b32_e32 v99, 0xffff0000, v201
	ds_read2st64_b32 v[200:201], v71 offset0:26 offset1:27
	ds_read2st64_b32 v[202:203], v71 offset0:28 offset1:29
	ds_read2st64_b32 v[204:205], v71 offset0:30 offset1:31
	v_mul_f32_e32 v128, v157, v128
	v_fma_f32 v178, v4, v72, -v128
	v_and_b32_e32 v128, 0xffff0000, v199
	v_mul_f32_e32 v128, v157, v128
	v_fma_f32 v176, v5, v73, -v128
	s_waitcnt lgkmcnt(2)
	v_lshlrev_b32_e32 v128, 16, v200
	v_mul_f32_e32 v128, v157, v128
	v_fma_f32 v169, v6, v68, -v128
	v_and_b32_e32 v128, 0xffff0000, v200
	v_mul_f32_e32 v128, v157, v128
	v_fma_f32 v166, v7, v80, -v128
	v_lshlrev_b32_e32 v128, 16, v201
	v_mul_f32_e32 v128, v157, v128
	v_fma_f32 v154, v8, v74, -v128
	v_and_b32_e32 v128, 0xffff0000, v201
	v_mul_f32_e32 v184, v147, v147
	v_mul_f32_e32 v128, v157, v128
	v_fmac_f32_e32 v184, v134, v134
	v_mul_f32_e32 v185, v144, v144
	v_mul_f32_e32 v181, v141, v141
	v_fma_f32 v152, v9, v75, -v128
	s_waitcnt lgkmcnt(1)
	v_lshlrev_b32_e32 v128, 16, v202
	v_fmac_f32_e32 v185, v130, v130
	v_fmac_f32_e32 v181, v125, v125
	v_fmac_f32_e32 v184, v168, v168
	v_mul_f32_e32 v128, v157, v128
	v_fmac_f32_e32 v185, v155, v155
	v_fmac_f32_e32 v181, v153, v153
	v_fmac_f32_e32 v184, v180, v180
	v_fma_f32 v149, v10, v81, -v128
	v_and_b32_e32 v128, 0xffff0000, v202
	v_fmac_f32_e32 v185, v178, v178
	v_fmac_f32_e32 v181, v176, v176
	v_mul_f32_e32 v128, v157, v128
	ds_bpermute_b32 v198, v188, v184
	v_mul_f32_e32 v174, v132, v132
	v_fma_f32 v146, v11, v82, -v128
	v_lshlrev_b32_e32 v128, 16, v203
	ds_bpermute_b32 v199, v188, v185
	ds_bpermute_b32 v200, v188, v181
	v_fmac_f32_e32 v174, v101, v101
	v_mul_f32_e32 v177, v127, v127
	v_mul_f32_e32 v179, v123, v123
	v_mul_f32_e32 v175, v120, v120
	v_mul_f32_e32 v128, v157, v128
	v_fmac_f32_e32 v177, v98, v98
	v_fmac_f32_e32 v179, v95, v95
	v_fmac_f32_e32 v175, v92, v92
	v_fmac_f32_e32 v174, v148, v148
	v_fma_f32 v143, v12, v76, -v128
	v_and_b32_e32 v128, 0xffff0000, v203
	v_fmac_f32_e32 v177, v145, v145
	v_fmac_f32_e32 v179, v142, v142
	v_fmac_f32_e32 v175, v137, v137
	v_fmac_f32_e32 v174, v166, v166
	v_mul_f32_e32 v128, v157, v128
	v_mul_f32_e32 v183, v150, v150
	v_fmac_f32_e32 v177, v154, v154
	v_fmac_f32_e32 v179, v152, v152
	v_fmac_f32_e32 v175, v149, v149
	v_fma_f32 v139, v13, v77, -v128
	s_waitcnt lgkmcnt(3)
	v_lshlrev_b32_e32 v128, 16, v204
	s_waitcnt lgkmcnt(2)
	v_add_f32_e32 v184, v184, v198
	ds_bpermute_b32 v198, v188, v174
	v_fmac_f32_e32 v183, v138, v138
	v_mul_f32_e32 v170, v97, v97
	v_mul_f32_e32 v128, v157, v128
	s_waitcnt lgkmcnt(2)
	v_add_f32_e32 v185, v185, v199
	s_waitcnt lgkmcnt(1)
	v_add_f32_e32 v181, v181, v200
	ds_bpermute_b32 v199, v188, v177
	ds_bpermute_b32 v200, v188, v179
	ds_bpermute_b32 v201, v188, v175
	v_fmac_f32_e32 v170, v88, v88
	v_mul_f32_e32 v172, v94, v94
	v_mul_f32_e32 v196, v96, v96
	v_mul_f32_e32 v195, v93, v93
	v_fmac_f32_e32 v183, v171, v171
	v_fma_f32 v140, v14, v69, -v128
	v_and_b32_e32 v128, 0xffff0000, v204
	v_fmac_f32_e32 v172, v87, v87
	v_fmac_f32_e32 v196, v86, v86
	v_fmac_f32_e32 v195, v85, v85
	v_fmac_f32_e32 v170, v129, v129
	v_fmac_f32_e32 v183, v182, v182
	v_mul_f32_e32 v128, v157, v128
	v_mul_f32_e32 v89, v157, v89
	v_fmac_f32_e32 v172, v124, v124
	v_fmac_f32_e32 v196, v126, v126
	v_fmac_f32_e32 v195, v122, v122
	v_fmac_f32_e32 v170, v143, v143
	v_fma_f32 v135, v15, v70, -v128
	v_lshlrev_b32_e32 v128, 16, v205
	ds_bpermute_b32 v197, v188, v183
	v_mul_f32_e32 v173, v136, v136
	v_fma_f32 v89, v49, v67, -v89
	v_fmac_f32_e32 v172, v139, v139
	v_fmac_f32_e32 v196, v140, v140
	v_fmac_f32_e32 v195, v135, v135
	v_mul_f32_e32 v128, v157, v128
	s_waitcnt lgkmcnt(4)
	v_add_f32_e32 v174, v174, v198
	ds_bpermute_b32 v198, v188, v170
	v_fmac_f32_e32 v173, v121, v121
	v_mul_f32_e32 v187, v89, v89
	v_mul_f32_e32 v99, v157, v99
	v_fma_f32 v131, v16, v66, -v128
	v_and_b32_e32 v128, 0xffff0000, v205
	s_waitcnt lgkmcnt(4)
	v_add_f32_e32 v177, v177, v199
	s_waitcnt lgkmcnt(3)
	v_add_f32_e32 v179, v179, v200
	s_waitcnt lgkmcnt(2)
	v_add_f32_e32 v175, v175, v201
	ds_bpermute_b32 v199, v188, v172
	ds_bpermute_b32 v200, v188, v196
	ds_bpermute_b32 v201, v188, v195
	v_fmac_f32_e32 v187, v83, v83
	v_fmac_f32_e32 v173, v151, v151
	v_fma_f32 v99, v65, v67, -v99
	v_mul_f32_e32 v128, v157, v128
	v_fmac_f32_e32 v187, v99, v99
	v_fmac_f32_e32 v173, v169, v169
	v_fma_f32 v128, v17, v67, -v128
	v_fmac_f32_e32 v187, v128, v128
	s_waitcnt lgkmcnt(4)
	v_add_f32_e32 v183, v183, v197
	ds_bpermute_b32 v197, v188, v173
	v_mul_f32_e32 v167, v100, v100
	s_waitcnt lgkmcnt(4)
	v_add_f32_e32 v170, v170, v198
	ds_bpermute_b32 v198, v188, v187
	v_fmac_f32_e32 v167, v90, v90
	s_waitcnt lgkmcnt(4)
	v_add_f32_e32 v172, v172, v199
	s_waitcnt lgkmcnt(3)
	v_add_f32_e32 v196, v196, v200
	s_waitcnt lgkmcnt(2)
	v_add_f32_e32 v195, v195, v201
	ds_bpermute_b32 v199, v189, v183
	ds_bpermute_b32 v200, v189, v184
	ds_bpermute_b32 v201, v189, v185
	v_fmac_f32_e32 v167, v133, v133
	v_fmac_f32_e32 v167, v146, v146
	s_waitcnt lgkmcnt(4)
	v_add_f32_e32 v173, v173, v197
	ds_bpermute_b32 v197, v188, v167
	v_mul_f32_e32 v186, v91, v91
	s_waitcnt lgkmcnt(4)
	v_add_f32_e32 v187, v187, v198
	ds_bpermute_b32 v198, v189, v173
	v_fmac_f32_e32 v186, v84, v84
	s_waitcnt lgkmcnt(4)
	v_add_f32_e32 v183, v183, v199
	s_waitcnt lgkmcnt(3)
	v_add_f32_e32 v184, v184, v200
	s_waitcnt lgkmcnt(2)
	v_add_f32_e32 v185, v185, v201
	ds_bpermute_b32 v199, v189, v174
	ds_bpermute_b32 v200, v189, v177
	ds_bpermute_b32 v201, v189, v179
	v_fmac_f32_e32 v186, v118, v118
	v_fmac_f32_e32 v186, v131, v131
	s_waitcnt lgkmcnt(4)
	v_add_f32_e32 v167, v167, v197
	ds_bpermute_b32 v197, v188, v186
	s_waitcnt lgkmcnt(4)
	v_add_f32_e32 v173, v173, v198
	ds_bpermute_b32 v198, v189, v167
	s_waitcnt lgkmcnt(4)
	v_add_f32_e32 v174, v174, v199
	s_waitcnt lgkmcnt(3)
	v_add_f32_e32 v177, v177, v200
	s_waitcnt lgkmcnt(2)
	v_add_f32_e32 v179, v179, v201
	ds_bpermute_b32 v199, v189, v170
	ds_bpermute_b32 v200, v189, v172
	ds_bpermute_b32 v201, v189, v196
	s_waitcnt lgkmcnt(4)
	v_add_f32_e32 v186, v186, v197
	ds_bpermute_b32 v197, v189, v181
	s_waitcnt lgkmcnt(4)
	v_add_f32_e32 v167, v167, v198
	ds_bpermute_b32 v198, v189, v186
	s_waitcnt lgkmcnt(4)
	v_add_f32_e32 v170, v170, v199
	s_waitcnt lgkmcnt(3)
	v_add_f32_e32 v172, v172, v200
	s_waitcnt lgkmcnt(2)
	v_add_f32_e32 v196, v196, v201
	ds_bpermute_b32 v199, v189, v187
	ds_bpermute_b32 v200, v190, v183
	ds_bpermute_b32 v201, v190, v184
	s_waitcnt lgkmcnt(4)
	v_add_f32_e32 v181, v181, v197
	ds_bpermute_b32 v197, v189, v175
	s_waitcnt lgkmcnt(4)
	v_add_f32_e32 v186, v186, v198
	ds_bpermute_b32 v198, v190, v181
	s_waitcnt lgkmcnt(4)
	v_add_f32_e32 v187, v187, v199
	s_waitcnt lgkmcnt(3)
	v_add_f32_e32 v183, v183, v200
	s_waitcnt lgkmcnt(2)
	v_add_f32_e32 v184, v184, v201
	ds_bpermute_b32 v199, v190, v173
	ds_bpermute_b32 v200, v190, v174
	ds_bpermute_b32 v201, v190, v177
	s_waitcnt lgkmcnt(4)
	v_add_f32_e32 v175, v175, v197
	s_waitcnt lgkmcnt(3)
	v_add_f32_e32 v181, v181, v198
	ds_bpermute_b32 v198, v190, v175
	s_waitcnt lgkmcnt(3)
	v_add_f32_e32 v173, v173, v199
	s_waitcnt lgkmcnt(2)
	v_add_f32_e32 v174, v174, v200
	s_waitcnt lgkmcnt(1)
	v_add_f32_e32 v177, v177, v201
	ds_bpermute_b32 v199, v190, v167
	ds_bpermute_b32 v200, v190, v170
	ds_bpermute_b32 v201, v190, v172
	s_waitcnt lgkmcnt(3)
	v_add_f32_e32 v175, v175, v198
	v_lshlrev_b32_e32 v198, 2, v165
	s_waitcnt lgkmcnt(2)
	v_add_f32_e32 v167, v167, v199
	s_waitcnt lgkmcnt(1)
	v_add_f32_e32 v170, v170, v200
	s_waitcnt lgkmcnt(0)
	v_add_f32_e32 v172, v172, v201
	global_load_dword v199, v198, s[4:5]
	global_load_dword v200, v198, s[4:5] offset:128
	global_load_dword v201, v198, s[4:5] offset:256
	ds_bpermute_b32 v197, v189, v195
	global_load_dword v198, v198, s[4:5] offset:384
	ds_bpermute_b32 v205, v191, v184
	ds_bpermute_b32 v202, v190, v186
	ds_bpermute_b32 v204, v191, v183
	s_waitcnt lgkmcnt(3)
	v_add_f32_e32 v195, v195, v197
	ds_bpermute_b32 v197, v190, v185
	s_waitcnt lgkmcnt(3)
	v_add_f32_e32 v184, v184, v205
	ds_bpermute_b32 v205, v191, v177
	s_waitcnt lgkmcnt(3)
	v_add_f32_e32 v186, v186, v202
	ds_bpermute_b32 v202, v191, v181
	s_waitcnt lgkmcnt(2)
	v_add_f32_e32 v185, v185, v197
	ds_bpermute_b32 v197, v190, v179
	ds_bpermute_b32 v203, v190, v187
	v_add_f32_e32 v183, v183, v204
	ds_bpermute_b32 v204, v191, v174
	s_waitcnt lgkmcnt(4)
	v_add_f32_e32 v177, v177, v205
	s_waitcnt lgkmcnt(2)
	v_add_f32_e32 v179, v179, v197
	ds_bpermute_b32 v197, v190, v196
	ds_bpermute_b32 v205, v191, v172
	v_add_f32_e32 v181, v181, v202
	ds_bpermute_b32 v202, v191, v175
	s_waitcnt lgkmcnt(4)
	v_add_f32_e32 v187, v187, v203
	s_waitcnt lgkmcnt(2)
	v_add_f32_e32 v196, v196, v197
	ds_bpermute_b32 v197, v190, v195
	ds_bpermute_b32 v203, v191, v173
	v_add_f32_e32 v174, v174, v204
	ds_bpermute_b32 v204, v191, v170
	s_waitcnt lgkmcnt(4)
	v_add_f32_e32 v172, v172, v205
	s_waitcnt lgkmcnt(2)
	v_add_f32_e32 v195, v195, v197
	ds_bpermute_b32 v197, v191, v185
	ds_bpermute_b32 v205, v192, v183
	v_add_f32_e32 v175, v175, v202
	ds_bpermute_b32 v202, v191, v195
	s_waitcnt lgkmcnt(4)
	v_add_f32_e32 v173, v173, v203
	s_waitcnt lgkmcnt(2)
	v_add_f32_e32 v185, v185, v197
	ds_bpermute_b32 v197, v191, v179
	ds_bpermute_b32 v203, v191, v167
	v_add_f32_e32 v170, v170, v204
	ds_bpermute_b32 v204, v191, v187
	s_waitcnt lgkmcnt(4)
	v_add_f32_e32 v205, v183, v205
	ds_bpermute_b32 v183, v192, v184
	s_waitcnt lgkmcnt(3)
	v_add_f32_e32 v179, v179, v197
	ds_bpermute_b32 v197, v191, v196
	v_add_f32_e32 v202, v195, v202
	ds_bpermute_b32 v195, v192, v173
	s_waitcnt lgkmcnt(4)
	v_add_f32_e32 v167, v167, v203
	ds_bpermute_b32 v203, v191, v186
	s_waitcnt lgkmcnt(4)
	v_add_f32_e32 v204, v187, v204
	ds_bpermute_b32 v187, v192, v181
	ds_bpermute_b32 v206, v192, v174
	s_waitcnt lgkmcnt(5)
	v_add_f32_e32 v207, v184, v183
	ds_bpermute_b32 v183, v192, v167
	s_waitcnt lgkmcnt(5)
	v_add_f32_e32 v197, v196, v197
	s_waitcnt lgkmcnt(4)
	v_add_f32_e32 v196, v173, v195
	ds_bpermute_b32 v173, v192, v177
	s_waitcnt lgkmcnt(4)
	v_add_f32_e32 v203, v186, v203
	ds_bpermute_b32 v186, v192, v185
	s_waitcnt lgkmcnt(4)
	v_add_f32_e32 v209, v181, v187
	ds_bpermute_b32 v181, v192, v175
	s_waitcnt lgkmcnt(4)
	v_add_f32_e32 v195, v174, v206
	ds_bpermute_b32 v206, v192, v170
	s_waitcnt lgkmcnt(4)
	v_add_f32_e32 v184, v167, v183
	ds_bpermute_b32 v167, v192, v172
	s_waitcnt lgkmcnt(4)
	v_add_f32_e32 v187, v177, v173
	ds_bpermute_b32 v173, v192, v202
	s_waitcnt lgkmcnt(4)
	v_add_f32_e32 v208, v185, v186
	ds_bpermute_b32 v174, v192, v179
	s_waitcnt lgkmcnt(4)
	v_add_f32_e32 v185, v175, v181
	ds_bpermute_b32 v175, v192, v204
	s_waitcnt lgkmcnt(4)
	v_add_f32_e32 v183, v170, v206
	ds_bpermute_b32 v170, v192, v197
	s_waitcnt lgkmcnt(4)
	v_add_f32_e32 v181, v172, v167
	v_fmamk_f32 v172, v205, 0x3c000000, v158
	s_mov_b32 s1, 0xf800000
	s_waitcnt lgkmcnt(3)
	v_add_f32_e32 v177, v202, v173
	v_mul_f32_e32 v173, 0x4f800000, v172
	v_cmp_gt_f32_e32 vcc, s1, v172
	s_waitcnt lgkmcnt(2)
	v_add_f32_e32 v186, v179, v174
	ds_bpermute_b32 v174, v192, v203
	s_waitcnt lgkmcnt(2)
	v_add_f32_e32 v167, v204, v175
	v_cndmask_b32_e32 v175, v172, v173, vcc
	s_waitcnt lgkmcnt(1)
	v_add_f32_e32 v179, v197, v170
	v_sqrt_f32_e32 v197, v175
	s_waitcnt lgkmcnt(0)
	v_add_f32_e32 v170, v203, v174
	s_waitcnt vmcnt(3)
	v_mul_f32_e32 v174, 0x3f4ccccd, v199
	s_waitcnt vmcnt(2)
	v_mul_f32_e32 v173, 0x3f4ccccd, v200
	v_add_u32_e32 v199, -1, v197
	v_fma_f32 v200, -v199, v197, v175
	v_cmp_ge_f32_e64 s[4:5], 0, v200
	v_add_u32_e32 v200, 1, v197
	s_waitcnt vmcnt(1)
	v_mul_f32_e32 v172, 0x3f4ccccd, v201
	v_cndmask_b32_e64 v199, v197, v199, s[4:5]
	v_fma_f32 v197, -v200, v197, v175
	v_cmp_lt_f32_e64 s[4:5], 0, v197
	v_lshlrev_b32_e32 v165, 1, v165
	v_lshlrev_b32_e32 v164, 10, v164
	v_cndmask_b32_e64 v197, v199, v200, s[4:5]
	v_mul_f32_e32 v199, 0x37800000, v197
	v_cndmask_b32_e32 v197, v197, v199, vcc
	v_cmp_class_f32_e32 vcc, v175, v159
	v_add3_u32 v164, s0, v165, v164
	s_waitcnt lgkmcnt(0)
	s_ashr_i32 s97, s96, 31
	v_cndmask_b32_e32 v197, v197, v175, vcc
	v_div_scale_f32 v199, s[4:5], v197, v197, 1.0
	v_rcp_f32_e32 v200, v199
	s_waitcnt vmcnt(0)
	v_mul_f32_e32 v175, 0x3f4ccccd, v198
	v_readlane_b32 s6, v254, 26
	v_readlane_b32 s7, v254, 27
	v_fma_f32 v198, -v199, v200, 1.0
	v_fmac_f32_e32 v200, v198, v200
	v_div_scale_f32 v198, vcc, 1.0, v197, 1.0
	v_mul_f32_e32 v201, v198, v200
	v_fma_f32 v202, -v199, v201, v198
	v_fmac_f32_e32 v201, v202, v200
	v_fma_f32 v198, -v199, v201, v198
	v_div_fmas_f32 v198, v198, v200, v201
	v_div_fixup_f32 v197, v198, v197, 1.0
	v_mul_f32_e32 v138, v138, v197
	v_mul_f32_e32 v138, v138, v174
	v_bfe_u32 v165, v138, 16, 1
	v_add3_u32 v138, v138, v165, s2
	ds_write_b16_d16_hi v164, v138
	v_mul_f32_e32 v138, v150, v197
	v_mul_f32_e32 v138, v138, v173
	v_bfe_u32 v150, v138, 16, 1
	v_add3_u32 v138, v138, v150, s2
	ds_write_b16_d16_hi v164, v138 offset:64
	v_mul_f32_e32 v138, v171, v197
	v_mul_f32_e32 v138, v138, v172
	v_bfe_u32 v150, v138, 16, 1
	v_add3_u32 v138, v138, v150, s2
	v_fmamk_f32 v150, v207, 0x3c000000, v158
	v_mul_f32_e32 v165, 0x4f800000, v150
	v_cmp_gt_f32_e32 vcc, s1, v150
	ds_write_b16_d16_hi v164, v138 offset:128
	v_mul_f32_e32 v138, v182, v197
	v_cndmask_b32_e32 v150, v150, v165, vcc
	v_sqrt_f32_e32 v165, v150
	v_mul_f32_e32 v138, v138, v175
	v_add_u32_e32 v171, -1, v165
	v_fma_f32 v182, -v171, v165, v150
	v_cmp_ge_f32_e64 s[4:5], 0, v182
	v_add_u32_e32 v182, 1, v165
	s_nop 0
	v_cndmask_b32_e64 v171, v165, v171, s[4:5]
	v_fma_f32 v165, -v182, v165, v150
	v_cmp_lt_f32_e64 s[4:5], 0, v165
	s_nop 1
	v_cndmask_b32_e64 v165, v171, v182, s[4:5]
	v_mul_f32_e32 v171, 0x37800000, v165
	v_cndmask_b32_e32 v165, v165, v171, vcc
	v_cmp_class_f32_e32 vcc, v150, v159
	v_bfe_u32 v182, v138, 16, 1
	v_add3_u32 v138, v138, v182, s2
	v_cndmask_b32_e32 v150, v165, v150, vcc
	v_div_scale_f32 v165, s[4:5], v150, v150, 1.0
	v_rcp_f32_e32 v171, v165
	ds_write_b16_d16_hi v164, v138 offset:192
	v_fma_f32 v138, -v165, v171, 1.0
	v_fmac_f32_e32 v171, v138, v171
	v_div_scale_f32 v138, vcc, 1.0, v150, 1.0
	v_mul_f32_e32 v182, v138, v171
	v_fma_f32 v197, -v165, v182, v138
	v_fmac_f32_e32 v182, v197, v171
	v_fma_f32 v138, -v165, v182, v138
	v_div_fmas_f32 v138, v138, v171, v182
	v_div_fixup_f32 v138, v138, v150, 1.0
	v_mul_f32_e32 v134, v134, v138
	v_mul_f32_e32 v134, v134, v174
	v_bfe_u32 v150, v134, 16, 1
	v_add3_u32 v134, v134, v150, s2
	ds_write_b16_d16_hi v164, v134 offset:256
	v_mul_f32_e32 v134, v147, v138
	v_mul_f32_e32 v134, v134, v173
	v_bfe_u32 v147, v134, 16, 1
	v_add3_u32 v134, v134, v147, s2
	ds_write_b16_d16_hi v164, v134 offset:320
	v_mul_f32_e32 v134, v168, v138
	v_mul_f32_e32 v134, v134, v172
	v_bfe_u32 v147, v134, 16, 1
	v_add3_u32 v134, v134, v147, s2
	v_fmamk_f32 v147, v208, 0x3c000000, v158
	v_mul_f32_e32 v150, 0x4f800000, v147
	v_cmp_gt_f32_e32 vcc, s1, v147
	ds_write_b16_d16_hi v164, v134 offset:384
	v_mul_f32_e32 v134, v180, v138
	v_cndmask_b32_e32 v147, v147, v150, vcc
	v_sqrt_f32_e32 v150, v147
	v_mul_f32_e32 v134, v134, v175
	v_add_u32_e32 v138, -1, v150
	v_fma_f32 v165, -v138, v150, v147
	v_cmp_ge_f32_e64 s[4:5], 0, v165
	v_add_u32_e32 v165, 1, v150
	s_nop 0
	v_cndmask_b32_e64 v138, v150, v138, s[4:5]
	v_fma_f32 v150, -v165, v150, v147
	v_cmp_lt_f32_e64 s[4:5], 0, v150
	s_nop 1
	v_cndmask_b32_e64 v138, v138, v165, s[4:5]
	v_mul_f32_e32 v150, 0x37800000, v138
	v_cndmask_b32_e32 v138, v138, v150, vcc
	v_cmp_class_f32_e32 vcc, v147, v159
	v_bfe_u32 v165, v134, 16, 1
	v_add3_u32 v134, v134, v165, s2
	v_cndmask_b32_e32 v138, v138, v147, vcc
	v_div_scale_f32 v147, s[4:5], v138, v138, 1.0
	v_rcp_f32_e32 v150, v147
	ds_write_b16_d16_hi v164, v134 offset:448
	v_fma_f32 v134, -v147, v150, 1.0
	v_fmac_f32_e32 v150, v134, v150
	v_div_scale_f32 v134, vcc, 1.0, v138, 1.0
	v_mul_f32_e32 v165, v134, v150
	v_fma_f32 v168, -v147, v165, v134
	v_fmac_f32_e32 v165, v168, v150
	v_fma_f32 v134, -v147, v165, v134
	v_div_fmas_f32 v134, v134, v150, v165
	v_div_fixup_f32 v134, v134, v138, 1.0
	v_mul_f32_e32 v130, v130, v134
	v_mul_f32_e32 v130, v130, v174
	v_bfe_u32 v138, v130, 16, 1
	v_add3_u32 v130, v130, v138, s2
	ds_write_b16_d16_hi v164, v130 offset:512
	v_mul_f32_e32 v130, v144, v134
	v_mul_f32_e32 v130, v130, v173
	v_bfe_u32 v138, v130, 16, 1
	v_add3_u32 v130, v130, v138, s2
	ds_write_b16_d16_hi v164, v130 offset:576
	v_mul_f32_e32 v130, v155, v134
	v_mul_f32_e32 v130, v130, v172
	v_bfe_u32 v138, v130, 16, 1
	v_add3_u32 v130, v130, v138, s2
	v_fmamk_f32 v138, v209, 0x3c000000, v158
	v_mul_f32_e32 v144, 0x4f800000, v138
	v_cmp_gt_f32_e32 vcc, s1, v138
	ds_write_b16_d16_hi v164, v130 offset:640
	v_mul_f32_e32 v130, v178, v134
	v_cndmask_b32_e32 v138, v138, v144, vcc
	v_sqrt_f32_e32 v144, v138
	v_mul_f32_e32 v130, v130, v175
	v_add_u32_e32 v134, -1, v144
	v_fma_f32 v147, -v134, v144, v138
	v_cmp_ge_f32_e64 s[4:5], 0, v147
	v_add_u32_e32 v147, 1, v144
	s_nop 0
	v_cndmask_b32_e64 v134, v144, v134, s[4:5]
	v_fma_f32 v144, -v147, v144, v138
	v_cmp_lt_f32_e64 s[4:5], 0, v144
	s_nop 1
	v_cndmask_b32_e64 v134, v134, v147, s[4:5]
	v_mul_f32_e32 v144, 0x37800000, v134
	v_cndmask_b32_e32 v134, v134, v144, vcc
	v_cmp_class_f32_e32 vcc, v138, v159
	v_bfe_u32 v147, v130, 16, 1
	v_add3_u32 v130, v130, v147, s2
	v_cndmask_b32_e32 v134, v134, v138, vcc
	v_div_scale_f32 v138, s[4:5], v134, v134, 1.0
	v_rcp_f32_e32 v144, v138
	ds_write_b16_d16_hi v164, v130 offset:704
	v_fma_f32 v130, -v138, v144, 1.0
	v_fmac_f32_e32 v144, v130, v144
	v_div_scale_f32 v130, vcc, 1.0, v134, 1.0
	v_mul_f32_e32 v147, v130, v144
	v_fma_f32 v150, -v138, v147, v130
	v_fmac_f32_e32 v147, v150, v144
	v_fma_f32 v130, -v138, v147, v130
	v_div_fmas_f32 v130, v130, v144, v147
	v_div_fixup_f32 v130, v130, v134, 1.0
	v_mul_f32_e32 v125, v125, v130
	v_mul_f32_e32 v125, v125, v174
	v_bfe_u32 v134, v125, 16, 1
	v_add3_u32 v125, v125, v134, s2
	ds_write_b16_d16_hi v164, v125 offset:768
	v_mul_f32_e32 v125, v141, v130
	v_mul_f32_e32 v125, v125, v173
	v_bfe_u32 v134, v125, 16, 1
	v_add3_u32 v125, v125, v134, s2
	ds_write_b16_d16_hi v164, v125 offset:832
	v_mul_f32_e32 v125, v153, v130
	v_mul_f32_e32 v125, v125, v172
	v_bfe_u32 v134, v125, 16, 1
	v_add3_u32 v125, v125, v134, s2
	v_fmamk_f32 v134, v196, 0x3c000000, v158
	v_mul_f32_e32 v138, 0x4f800000, v134
	v_cmp_gt_f32_e32 vcc, s1, v134
	ds_write_b16_d16_hi v164, v125 offset:896
	v_mul_f32_e32 v125, v176, v130
	v_cndmask_b32_e32 v134, v134, v138, vcc
	v_sqrt_f32_e32 v138, v134
	v_mul_f32_e32 v125, v125, v175
	v_add_u32_e32 v130, -1, v138
	v_fma_f32 v141, -v130, v138, v134
	v_cmp_ge_f32_e64 s[4:5], 0, v141
	v_add_u32_e32 v141, 1, v138
	s_nop 0
	v_cndmask_b32_e64 v130, v138, v130, s[4:5]
	v_fma_f32 v138, -v141, v138, v134
	v_cmp_lt_f32_e64 s[4:5], 0, v138
	s_nop 1
	v_cndmask_b32_e64 v130, v130, v141, s[4:5]
	v_mul_f32_e32 v138, 0x37800000, v130
	v_cndmask_b32_e32 v130, v130, v138, vcc
	v_cmp_class_f32_e32 vcc, v134, v159
	v_bfe_u32 v141, v125, 16, 1
	v_add3_u32 v125, v125, v141, s2
	v_cndmask_b32_e32 v130, v130, v134, vcc
	v_div_scale_f32 v134, s[4:5], v130, v130, 1.0
	v_rcp_f32_e32 v138, v134
	ds_write_b16_d16_hi v164, v125 offset:960
	v_fma_f32 v125, -v134, v138, 1.0
	v_fmac_f32_e32 v138, v125, v138
	v_div_scale_f32 v125, vcc, 1.0, v130, 1.0
	v_mul_f32_e32 v141, v125, v138
	v_fma_f32 v144, -v134, v141, v125
	v_fmac_f32_e32 v141, v144, v138
	v_fma_f32 v125, -v134, v141, v125
	v_div_fmas_f32 v125, v125, v138, v141
	v_div_fixup_f32 v125, v125, v130, 1.0
	v_mul_f32_e32 v121, v121, v125
	v_mul_f32_e32 v121, v121, v174
	v_bfe_u32 v130, v121, 16, 1
	v_add3_u32 v121, v121, v130, s2
	ds_write_b16_d16_hi v164, v121 offset:2048
	v_mul_f32_e32 v121, v136, v125
	v_mul_f32_e32 v121, v121, v173
	v_bfe_u32 v130, v121, 16, 1
	v_add3_u32 v121, v121, v130, s2
	ds_write_b16_d16_hi v164, v121 offset:2112
	v_mul_f32_e32 v121, v151, v125
	v_mul_f32_e32 v121, v121, v172
	v_bfe_u32 v130, v121, 16, 1
	v_add3_u32 v121, v121, v130, s2
	v_fmamk_f32 v130, v195, 0x3c000000, v158
	v_mul_f32_e32 v134, 0x4f800000, v130
	v_cmp_gt_f32_e32 vcc, s1, v130
	ds_write_b16_d16_hi v164, v121 offset:2176
	v_mul_f32_e32 v121, v169, v125
	v_cndmask_b32_e32 v130, v130, v134, vcc
	v_sqrt_f32_e32 v134, v130
	v_mul_f32_e32 v121, v121, v175
	v_add_u32_e32 v125, -1, v134
	v_fma_f32 v136, -v125, v134, v130
	v_cmp_ge_f32_e64 s[4:5], 0, v136
	v_add_u32_e32 v136, 1, v134
	s_nop 0
	v_cndmask_b32_e64 v125, v134, v125, s[4:5]
	v_fma_f32 v134, -v136, v134, v130
	v_cmp_lt_f32_e64 s[4:5], 0, v134
	s_nop 1
	v_cndmask_b32_e64 v125, v125, v136, s[4:5]
	v_mul_f32_e32 v134, 0x37800000, v125
	v_cndmask_b32_e32 v125, v125, v134, vcc
	v_cmp_class_f32_e32 vcc, v130, v159
	v_bfe_u32 v136, v121, 16, 1
	v_add3_u32 v121, v121, v136, s2
	v_cndmask_b32_e32 v125, v125, v130, vcc
	v_div_scale_f32 v130, s[4:5], v125, v125, 1.0
	v_rcp_f32_e32 v134, v130
	ds_write_b16_d16_hi v164, v121 offset:2240
	v_fma_f32 v121, -v130, v134, 1.0
	v_fmac_f32_e32 v134, v121, v134
	v_div_scale_f32 v121, vcc, 1.0, v125, 1.0
	v_mul_f32_e32 v136, v121, v134
	v_fma_f32 v138, -v130, v136, v121
	v_fmac_f32_e32 v136, v138, v134
	v_fma_f32 v121, -v130, v136, v121
	v_div_fmas_f32 v121, v121, v134, v136
	v_div_fixup_f32 v121, v121, v125, 1.0
	v_mul_f32_e32 v101, v101, v121
	v_mul_f32_e32 v101, v101, v174
	v_bfe_u32 v125, v101, 16, 1
	v_add3_u32 v101, v101, v125, s2
	ds_write_b16_d16_hi v164, v101 offset:2304
	v_mul_f32_e32 v101, v132, v121
	v_mul_f32_e32 v101, v101, v173
	v_bfe_u32 v125, v101, 16, 1
	v_add3_u32 v101, v101, v125, s2
	ds_write_b16_d16_hi v164, v101 offset:2368
	v_mul_f32_e32 v101, v148, v121
	v_mul_f32_e32 v101, v101, v172
	v_bfe_u32 v125, v101, 16, 1
	v_add3_u32 v101, v101, v125, s2
	v_fmamk_f32 v125, v187, 0x3c000000, v158
	v_mul_f32_e32 v130, 0x4f800000, v125
	v_cmp_gt_f32_e32 vcc, s1, v125
	ds_write_b16_d16_hi v164, v101 offset:2432
	v_mul_f32_e32 v101, v166, v121
	v_cndmask_b32_e32 v125, v125, v130, vcc
	v_sqrt_f32_e32 v130, v125
	v_mul_f32_e32 v101, v101, v175
	v_add_u32_e32 v121, -1, v130
	v_fma_f32 v132, -v121, v130, v125
	v_cmp_ge_f32_e64 s[4:5], 0, v132
	v_add_u32_e32 v132, 1, v130
	s_nop 0
	v_cndmask_b32_e64 v121, v130, v121, s[4:5]
	v_fma_f32 v130, -v132, v130, v125
	v_cmp_lt_f32_e64 s[4:5], 0, v130
	s_nop 1
	v_cndmask_b32_e64 v121, v121, v132, s[4:5]
	v_mul_f32_e32 v130, 0x37800000, v121
	v_cndmask_b32_e32 v121, v121, v130, vcc
	v_cmp_class_f32_e32 vcc, v125, v159
	v_bfe_u32 v132, v101, 16, 1
	v_add3_u32 v101, v101, v132, s2
	v_cndmask_b32_e32 v121, v121, v125, vcc
	v_div_scale_f32 v125, s[4:5], v121, v121, 1.0
	v_rcp_f32_e32 v130, v125
	ds_write_b16_d16_hi v164, v101 offset:2496
	v_fma_f32 v101, -v125, v130, 1.0
	v_fmac_f32_e32 v130, v101, v130
	v_div_scale_f32 v101, vcc, 1.0, v121, 1.0
	v_mul_f32_e32 v132, v101, v130
	v_fma_f32 v134, -v125, v132, v101
	v_fmac_f32_e32 v132, v134, v130
	v_fma_f32 v101, -v125, v132, v101
	v_div_fmas_f32 v101, v101, v130, v132
	v_div_fixup_f32 v101, v101, v121, 1.0
	v_mul_f32_e32 v98, v98, v101
	v_mul_f32_e32 v98, v98, v174
	v_bfe_u32 v121, v98, 16, 1
	v_add3_u32 v98, v98, v121, s2
	ds_write_b16_d16_hi v164, v98 offset:2560
	v_mul_f32_e32 v98, v127, v101
	v_mul_f32_e32 v98, v98, v173
	v_bfe_u32 v121, v98, 16, 1
	v_add3_u32 v98, v98, v121, s2
	ds_write_b16_d16_hi v164, v98 offset:2624
	v_mul_f32_e32 v98, v145, v101
	v_mul_f32_e32 v98, v98, v172
	v_bfe_u32 v121, v98, 16, 1
	v_add3_u32 v98, v98, v121, s2
	v_fmamk_f32 v121, v186, 0x3c000000, v158
	v_mul_f32_e32 v125, 0x4f800000, v121
	v_cmp_gt_f32_e32 vcc, s1, v121
	ds_write_b16_d16_hi v164, v98 offset:2688
	v_mul_f32_e32 v98, v154, v101
	v_cndmask_b32_e32 v121, v121, v125, vcc
	v_sqrt_f32_e32 v125, v121
	v_mul_f32_e32 v98, v98, v175
	v_add_u32_e32 v101, -1, v125
	v_fma_f32 v127, -v101, v125, v121
	v_cmp_ge_f32_e64 s[4:5], 0, v127
	v_add_u32_e32 v127, 1, v125
	s_nop 0
	v_cndmask_b32_e64 v101, v125, v101, s[4:5]
	v_fma_f32 v125, -v127, v125, v121
	v_cmp_lt_f32_e64 s[4:5], 0, v125
	s_nop 1
	v_cndmask_b32_e64 v101, v101, v127, s[4:5]
	v_mul_f32_e32 v125, 0x37800000, v101
	v_cndmask_b32_e32 v101, v101, v125, vcc
	v_cmp_class_f32_e32 vcc, v121, v159
	v_bfe_u32 v127, v98, 16, 1
	v_add3_u32 v98, v98, v127, s2
	v_cndmask_b32_e32 v101, v101, v121, vcc
	v_div_scale_f32 v121, s[4:5], v101, v101, 1.0
	v_rcp_f32_e32 v125, v121
	ds_write_b16_d16_hi v164, v98 offset:2752
	v_fma_f32 v98, -v121, v125, 1.0
	v_fmac_f32_e32 v125, v98, v125
	v_div_scale_f32 v98, vcc, 1.0, v101, 1.0
	v_mul_f32_e32 v127, v98, v125
	v_fma_f32 v130, -v121, v127, v98
	v_fmac_f32_e32 v127, v130, v125
	v_fma_f32 v98, -v121, v127, v98
	v_div_fmas_f32 v98, v98, v125, v127
	v_div_fixup_f32 v98, v98, v101, 1.0
	v_mul_f32_e32 v95, v95, v98
	v_mul_f32_e32 v95, v95, v174
	v_bfe_u32 v101, v95, 16, 1
	v_add3_u32 v95, v95, v101, s2
	ds_write_b16_d16_hi v164, v95 offset:2816
	v_mul_f32_e32 v95, v123, v98
	v_mul_f32_e32 v95, v95, v173
	v_bfe_u32 v101, v95, 16, 1
	v_add3_u32 v95, v95, v101, s2
	ds_write_b16_d16_hi v164, v95 offset:2880
	v_mul_f32_e32 v95, v142, v98
	v_mul_f32_e32 v95, v95, v172
	v_bfe_u32 v101, v95, 16, 1
	v_add3_u32 v95, v95, v101, s2
	v_fmamk_f32 v101, v185, 0x3c000000, v158
	v_mul_f32_e32 v121, 0x4f800000, v101
	v_cmp_gt_f32_e32 vcc, s1, v101
	ds_write_b16_d16_hi v164, v95 offset:2944
	v_mul_f32_e32 v95, v152, v98
	v_cndmask_b32_e32 v101, v101, v121, vcc
	v_sqrt_f32_e32 v121, v101
	v_mul_f32_e32 v95, v95, v175
	v_add_u32_e32 v98, -1, v121
	v_fma_f32 v123, -v98, v121, v101
	v_cmp_ge_f32_e64 s[4:5], 0, v123
	v_add_u32_e32 v123, 1, v121
	s_nop 0
	v_cndmask_b32_e64 v98, v121, v98, s[4:5]
	v_fma_f32 v121, -v123, v121, v101
	v_cmp_lt_f32_e64 s[4:5], 0, v121
	s_nop 1
	v_cndmask_b32_e64 v98, v98, v123, s[4:5]
	v_mul_f32_e32 v121, 0x37800000, v98
	v_cndmask_b32_e32 v98, v98, v121, vcc
	v_cmp_class_f32_e32 vcc, v101, v159
	v_bfe_u32 v123, v95, 16, 1
	v_add3_u32 v95, v95, v123, s2
	v_cndmask_b32_e32 v98, v98, v101, vcc
	v_div_scale_f32 v101, s[4:5], v98, v98, 1.0
	v_rcp_f32_e32 v121, v101
	ds_write_b16_d16_hi v164, v95 offset:3008
	v_fma_f32 v95, -v101, v121, 1.0
	v_fmac_f32_e32 v121, v95, v121
	v_div_scale_f32 v95, vcc, 1.0, v98, 1.0
	v_mul_f32_e32 v123, v95, v121
	v_fma_f32 v125, -v101, v123, v95
	v_fmac_f32_e32 v123, v125, v121
	v_fma_f32 v95, -v101, v123, v95
	v_div_fmas_f32 v95, v95, v121, v123
	v_div_fixup_f32 v95, v95, v98, 1.0
	v_mul_f32_e32 v92, v92, v95
	v_mul_f32_e32 v92, v92, v174
	v_bfe_u32 v98, v92, 16, 1
	v_add3_u32 v92, v92, v98, s2
	ds_write_b16_d16_hi v164, v92 offset:4096
	v_mul_f32_e32 v92, v120, v95
	v_mul_f32_e32 v92, v92, v173
	v_bfe_u32 v98, v92, 16, 1
	v_add3_u32 v92, v92, v98, s2
	ds_write_b16_d16_hi v164, v92 offset:4160
	v_mul_f32_e32 v92, v137, v95
	v_mul_f32_e32 v92, v92, v172
	v_bfe_u32 v98, v92, 16, 1
	v_add3_u32 v92, v92, v98, s2
	v_fmamk_f32 v98, v184, 0x3c000000, v158
	v_mul_f32_e32 v101, 0x4f800000, v98
	v_cmp_gt_f32_e32 vcc, s1, v98
	ds_write_b16_d16_hi v164, v92 offset:4224
	v_mul_f32_e32 v92, v149, v95
	v_cndmask_b32_e32 v98, v98, v101, vcc
	v_sqrt_f32_e32 v101, v98
	v_mul_f32_e32 v92, v92, v175
	v_add_u32_e32 v95, -1, v101
	v_fma_f32 v120, -v95, v101, v98
	v_cmp_ge_f32_e64 s[4:5], 0, v120
	v_add_u32_e32 v120, 1, v101
	s_nop 0
	v_cndmask_b32_e64 v95, v101, v95, s[4:5]
	v_fma_f32 v101, -v120, v101, v98
	v_cmp_lt_f32_e64 s[4:5], 0, v101
	s_nop 1
	v_cndmask_b32_e64 v95, v95, v120, s[4:5]
	v_mul_f32_e32 v101, 0x37800000, v95
	v_cndmask_b32_e32 v95, v95, v101, vcc
	v_cmp_class_f32_e32 vcc, v98, v159
	v_bfe_u32 v120, v92, 16, 1
	v_add3_u32 v92, v92, v120, s2
	v_cndmask_b32_e32 v95, v95, v98, vcc
	v_div_scale_f32 v98, s[4:5], v95, v95, 1.0
	v_rcp_f32_e32 v101, v98
	ds_write_b16_d16_hi v164, v92 offset:4288
	v_fma_f32 v92, -v98, v101, 1.0
	v_fmac_f32_e32 v101, v92, v101
	v_div_scale_f32 v92, vcc, 1.0, v95, 1.0
	v_mul_f32_e32 v120, v92, v101
	v_fma_f32 v121, -v98, v120, v92
	v_fmac_f32_e32 v120, v121, v101
	v_fma_f32 v92, -v98, v120, v92
	v_div_fmas_f32 v92, v92, v101, v120
	v_div_fixup_f32 v92, v92, v95, 1.0
	v_mul_f32_e32 v90, v90, v92
	v_mul_f32_e32 v90, v90, v174
	v_bfe_u32 v95, v90, 16, 1
	v_add3_u32 v90, v90, v95, s2
	ds_write_b16_d16_hi v164, v90 offset:4352
	v_mul_f32_e32 v90, v100, v92
	v_mul_f32_e32 v90, v90, v173
	v_bfe_u32 v95, v90, 16, 1
	v_add3_u32 v90, v90, v95, s2
	ds_write_b16_d16_hi v164, v90 offset:4416
	v_mul_f32_e32 v90, v133, v92
	v_mul_f32_e32 v90, v90, v172
	v_bfe_u32 v95, v90, 16, 1
	v_add3_u32 v90, v90, v95, s2
	v_fmamk_f32 v95, v183, 0x3c000000, v158
	v_mul_f32_e32 v98, 0x4f800000, v95
	v_cmp_gt_f32_e32 vcc, s1, v95
	ds_write_b16_d16_hi v164, v90 offset:4480
	v_mul_f32_e32 v90, v146, v92
	v_cndmask_b32_e32 v95, v95, v98, vcc
	v_sqrt_f32_e32 v98, v95
	v_mul_f32_e32 v90, v90, v175
	v_add_u32_e32 v92, -1, v98
	v_fma_f32 v100, -v92, v98, v95
	v_cmp_ge_f32_e64 s[4:5], 0, v100
	v_add_u32_e32 v100, 1, v98
	s_nop 0
	v_cndmask_b32_e64 v92, v98, v92, s[4:5]
	v_fma_f32 v98, -v100, v98, v95
	v_cmp_lt_f32_e64 s[4:5], 0, v98
	s_nop 1
	v_cndmask_b32_e64 v92, v92, v100, s[4:5]
	v_mul_f32_e32 v98, 0x37800000, v92
	v_cndmask_b32_e32 v92, v92, v98, vcc
	v_cmp_class_f32_e32 vcc, v95, v159
	v_bfe_u32 v100, v90, 16, 1
	v_add3_u32 v90, v90, v100, s2
	v_cndmask_b32_e32 v92, v92, v95, vcc
	v_div_scale_f32 v95, s[4:5], v92, v92, 1.0
	v_rcp_f32_e32 v98, v95
	ds_write_b16_d16_hi v164, v90 offset:4544
	v_fma_f32 v90, -v95, v98, 1.0
	v_fmac_f32_e32 v98, v90, v98
	v_div_scale_f32 v90, vcc, 1.0, v92, 1.0
	v_mul_f32_e32 v100, v90, v98
	v_fma_f32 v101, -v95, v100, v90
	v_fmac_f32_e32 v100, v101, v98
	v_fma_f32 v90, -v95, v100, v90
	v_div_fmas_f32 v90, v90, v98, v100
	v_div_fixup_f32 v90, v90, v92, 1.0
	v_mul_f32_e32 v88, v88, v90
	v_mul_f32_e32 v88, v174, v88
	v_bfe_u32 v92, v88, 16, 1
	v_add3_u32 v88, v88, v92, s2
	ds_write_b16_d16_hi v164, v88 offset:4608
	v_mul_f32_e32 v88, v97, v90
	v_mul_f32_e32 v88, v88, v173
	v_bfe_u32 v92, v88, 16, 1
	v_add3_u32 v88, v88, v92, s2
	ds_write_b16_d16_hi v164, v88 offset:4672
	v_mul_f32_e32 v88, v129, v90
	v_mul_f32_e32 v88, v88, v172
	v_bfe_u32 v92, v88, 16, 1
	v_add3_u32 v88, v88, v92, s2
	v_fmamk_f32 v92, v181, 0x3c000000, v158
	v_mul_f32_e32 v95, 0x4f800000, v92
	v_cmp_gt_f32_e32 vcc, s1, v92
	ds_write_b16_d16_hi v164, v88 offset:4736
	v_mul_f32_e32 v88, v143, v90
	v_cndmask_b32_e32 v92, v92, v95, vcc
	v_sqrt_f32_e32 v95, v92
	v_mul_f32_e32 v88, v88, v175
	v_add_u32_e32 v90, -1, v95
	v_fma_f32 v97, -v90, v95, v92
	v_cmp_ge_f32_e64 s[4:5], 0, v97
	v_add_u32_e32 v97, 1, v95
	s_nop 0
	v_cndmask_b32_e64 v90, v95, v90, s[4:5]
	v_fma_f32 v95, -v97, v95, v92
	v_cmp_lt_f32_e64 s[4:5], 0, v95
	s_nop 1
	v_cndmask_b32_e64 v90, v90, v97, s[4:5]
	v_mul_f32_e32 v95, 0x37800000, v90
	v_cndmask_b32_e32 v90, v90, v95, vcc
	v_cmp_class_f32_e32 vcc, v92, v159
	v_bfe_u32 v97, v88, 16, 1
	v_add3_u32 v88, v88, v97, s2
	v_cndmask_b32_e32 v90, v90, v92, vcc
	v_div_scale_f32 v92, s[4:5], v90, v90, 1.0
	v_rcp_f32_e32 v95, v92
	ds_write_b16_d16_hi v164, v88 offset:4800
	v_fma_f32 v88, -v92, v95, 1.0
	v_fmac_f32_e32 v95, v88, v95
	v_div_scale_f32 v88, vcc, 1.0, v90, 1.0
	v_mul_f32_e32 v97, v88, v95
	v_fma_f32 v98, -v92, v97, v88
	v_fmac_f32_e32 v97, v98, v95
	v_fma_f32 v88, -v92, v97, v88
	v_div_fmas_f32 v88, v88, v95, v97
	v_div_fixup_f32 v88, v88, v90, 1.0
	v_mul_f32_e32 v87, v87, v88
	v_mul_f32_e32 v87, v174, v87
	v_bfe_u32 v90, v87, 16, 1
	v_add3_u32 v87, v87, v90, s2
	ds_write_b16_d16_hi v164, v87 offset:4864
	v_mul_f32_e32 v87, v94, v88
	v_mul_f32_e32 v87, v173, v87
	v_bfe_u32 v90, v87, 16, 1
	v_add3_u32 v87, v87, v90, s2
	ds_write_b16_d16_hi v164, v87 offset:4928
	v_mul_f32_e32 v87, v124, v88
	v_mul_f32_e32 v87, v87, v172
	v_bfe_u32 v90, v87, 16, 1
	v_add3_u32 v87, v87, v90, s2
	v_fmamk_f32 v90, v179, 0x3c000000, v158
	v_mul_f32_e32 v92, 0x4f800000, v90
	v_cmp_gt_f32_e32 vcc, s1, v90
	ds_write_b16_d16_hi v164, v87 offset:4992
	v_mul_f32_e32 v87, v139, v88
	v_cndmask_b32_e32 v90, v90, v92, vcc
	v_sqrt_f32_e32 v92, v90
	v_mul_f32_e32 v87, v87, v175
	v_add_u32_e32 v88, -1, v92
	v_fma_f32 v94, -v88, v92, v90
	v_cmp_ge_f32_e64 s[4:5], 0, v94
	v_add_u32_e32 v94, 1, v92
	s_nop 0
	v_cndmask_b32_e64 v88, v92, v88, s[4:5]
	v_fma_f32 v92, -v94, v92, v90
	v_cmp_lt_f32_e64 s[4:5], 0, v92
	s_nop 1
	v_cndmask_b32_e64 v88, v88, v94, s[4:5]
	v_mul_f32_e32 v92, 0x37800000, v88
	v_cndmask_b32_e32 v88, v88, v92, vcc
	v_cmp_class_f32_e32 vcc, v90, v159
	v_bfe_u32 v94, v87, 16, 1
	v_add3_u32 v87, v87, v94, s2
	v_cndmask_b32_e32 v88, v88, v90, vcc
	v_div_scale_f32 v90, s[4:5], v88, v88, 1.0
	v_rcp_f32_e32 v92, v90
	ds_write_b16_d16_hi v164, v87 offset:5056
	v_fma_f32 v87, -v90, v92, 1.0
	v_fmac_f32_e32 v92, v87, v92
	v_div_scale_f32 v87, vcc, 1.0, v88, 1.0
	v_mul_f32_e32 v94, v87, v92
	v_fma_f32 v95, -v90, v94, v87
	v_fmac_f32_e32 v94, v95, v92
	v_fma_f32 v87, -v90, v94, v87
	v_div_fmas_f32 v87, v87, v92, v94
	v_div_fixup_f32 v87, v87, v88, 1.0
	v_mul_f32_e32 v86, v86, v87
	v_mul_f32_e32 v86, v174, v86
	v_bfe_u32 v88, v86, 16, 1
	v_add3_u32 v86, v86, v88, s2
	ds_write_b16_d16_hi v164, v86 offset:6144
	v_mul_f32_e32 v86, v96, v87
	v_mul_f32_e32 v86, v173, v86
	v_bfe_u32 v88, v86, 16, 1
	v_add3_u32 v86, v86, v88, s2
	ds_write_b16_d16_hi v164, v86 offset:6208
	v_mul_f32_e32 v86, v126, v87
	v_mul_f32_e32 v86, v172, v86
	v_bfe_u32 v88, v86, 16, 1
	v_add3_u32 v86, v86, v88, s2
	v_fmamk_f32 v88, v177, 0x3c000000, v158
	v_mul_f32_e32 v90, 0x4f800000, v88
	v_cmp_gt_f32_e32 vcc, s1, v88
	ds_write_b16_d16_hi v164, v86 offset:6272
	v_mul_f32_e32 v86, v140, v87
	v_cndmask_b32_e32 v88, v88, v90, vcc
	v_sqrt_f32_e32 v90, v88
	v_mul_f32_e32 v86, v86, v175
	v_add_u32_e32 v87, -1, v90
	v_fma_f32 v92, -v87, v90, v88
	v_cmp_ge_f32_e64 s[4:5], 0, v92
	v_add_u32_e32 v92, 1, v90
	s_nop 0
	v_cndmask_b32_e64 v87, v90, v87, s[4:5]
	v_fma_f32 v90, -v92, v90, v88
	v_cmp_lt_f32_e64 s[4:5], 0, v90
	s_nop 1
	v_cndmask_b32_e64 v87, v87, v92, s[4:5]
	v_mul_f32_e32 v90, 0x37800000, v87
	v_cndmask_b32_e32 v87, v87, v90, vcc
	v_cmp_class_f32_e32 vcc, v88, v159
	v_bfe_u32 v92, v86, 16, 1
	v_add3_u32 v86, v86, v92, s2
	v_cndmask_b32_e32 v87, v87, v88, vcc
	v_div_scale_f32 v88, s[4:5], v87, v87, 1.0
	v_rcp_f32_e32 v90, v88
	ds_write_b16_d16_hi v164, v86 offset:6336
	v_fma_f32 v86, -v88, v90, 1.0
	v_fmac_f32_e32 v90, v86, v90
	v_div_scale_f32 v86, vcc, 1.0, v87, 1.0
	v_mul_f32_e32 v92, v86, v90
	v_fma_f32 v94, -v88, v92, v86
	v_fmac_f32_e32 v92, v94, v90
	v_fma_f32 v86, -v88, v92, v86
	v_div_fmas_f32 v86, v86, v90, v92
	v_div_fixup_f32 v86, v86, v87, 1.0
	v_mul_f32_e32 v85, v85, v86
	v_mul_f32_e32 v85, v174, v85
	v_bfe_u32 v87, v85, 16, 1
	v_add3_u32 v85, v85, v87, s2
	ds_write_b16_d16_hi v164, v85 offset:6400
	v_mul_f32_e32 v85, v93, v86
	v_mul_f32_e32 v85, v173, v85
	v_bfe_u32 v87, v85, 16, 1
	v_add3_u32 v85, v85, v87, s2
	ds_write_b16_d16_hi v164, v85 offset:6464
	v_mul_f32_e32 v85, v122, v86
	v_mul_f32_e32 v85, v172, v85
	v_bfe_u32 v87, v85, 16, 1
	v_add3_u32 v85, v85, v87, s2
	v_fmamk_f32 v87, v170, 0x3c000000, v158
	v_mul_f32_e32 v88, 0x4f800000, v87
	v_cmp_gt_f32_e32 vcc, s1, v87
	ds_write_b16_d16_hi v164, v85 offset:6528
	v_mul_f32_e32 v85, v135, v86
	v_cndmask_b32_e32 v87, v87, v88, vcc
	v_sqrt_f32_e32 v88, v87
	v_mul_f32_e32 v85, v175, v85
	v_add_u32_e32 v86, -1, v88
	v_fma_f32 v90, -v86, v88, v87
	v_cmp_ge_f32_e64 s[4:5], 0, v90
	v_add_u32_e32 v90, 1, v88
	s_nop 0
	v_cndmask_b32_e64 v86, v88, v86, s[4:5]
	v_fma_f32 v88, -v90, v88, v87
	v_cmp_lt_f32_e64 s[4:5], 0, v88
	s_nop 1
	v_cndmask_b32_e64 v86, v86, v90, s[4:5]
	v_mul_f32_e32 v88, 0x37800000, v86
	v_cndmask_b32_e32 v86, v86, v88, vcc
	v_cmp_class_f32_e32 vcc, v87, v159
	v_bfe_u32 v90, v85, 16, 1
	v_add3_u32 v85, v85, v90, s2
	v_cndmask_b32_e32 v86, v86, v87, vcc
	v_div_scale_f32 v87, s[4:5], v86, v86, 1.0
	v_rcp_f32_e32 v88, v87
	ds_write_b16_d16_hi v164, v85 offset:6592
	v_fma_f32 v85, -v87, v88, 1.0
	v_fmac_f32_e32 v88, v85, v88
	v_div_scale_f32 v85, vcc, 1.0, v86, 1.0
	v_mul_f32_e32 v90, v85, v88
	v_fma_f32 v92, -v87, v90, v85
	v_fmac_f32_e32 v90, v92, v88
	v_fma_f32 v85, -v87, v90, v85
	v_div_fmas_f32 v85, v85, v88, v90
	v_div_fixup_f32 v85, v85, v86, 1.0
	v_mul_f32_e32 v84, v84, v85
	v_mul_f32_e32 v84, v174, v84
	v_bfe_u32 v86, v84, 16, 1
	v_add3_u32 v84, v84, v86, s2
	ds_write_b16_d16_hi v164, v84 offset:6656
	v_mul_f32_e32 v84, v91, v85
	v_mul_f32_e32 v84, v173, v84
	v_bfe_u32 v86, v84, 16, 1
	v_add3_u32 v84, v84, v86, s2
	ds_write_b16_d16_hi v164, v84 offset:6720
	v_mul_f32_e32 v84, v118, v85
	v_mul_f32_e32 v84, v172, v84
	v_bfe_u32 v86, v84, 16, 1
	v_add3_u32 v84, v84, v86, s2
	v_fmamk_f32 v86, v167, 0x3c000000, v158
	v_mul_f32_e32 v87, 0x4f800000, v86
	v_cmp_gt_f32_e32 vcc, s1, v86
	ds_write_b16_d16_hi v164, v84 offset:6784
	v_mul_f32_e32 v84, v131, v85
	v_cndmask_b32_e32 v86, v86, v87, vcc
	v_sqrt_f32_e32 v87, v86
	v_mul_f32_e32 v84, v175, v84
	v_add_u32_e32 v85, -1, v87
	v_fma_f32 v88, -v85, v87, v86
	v_cmp_ge_f32_e64 s[4:5], 0, v88
	v_add_u32_e32 v88, 1, v87
	s_nop 0
	v_cndmask_b32_e64 v85, v87, v85, s[4:5]
	v_fma_f32 v87, -v88, v87, v86
	v_cmp_lt_f32_e64 s[4:5], 0, v87
	s_nop 1
	v_cndmask_b32_e64 v85, v85, v88, s[4:5]
	v_mul_f32_e32 v87, 0x37800000, v85
	v_cndmask_b32_e32 v85, v85, v87, vcc
	v_cmp_class_f32_e32 vcc, v86, v159
	v_bfe_u32 v88, v84, 16, 1
	v_add3_u32 v84, v84, v88, s2
	v_cndmask_b32_e32 v85, v85, v86, vcc
	v_div_scale_f32 v86, s[4:5], v85, v85, 1.0
	v_rcp_f32_e32 v87, v86
	ds_write_b16_d16_hi v164, v84 offset:6848
	s_lshl_b64 s[4:5], s[96:97], 11
	s_add_u32 s4, s6, s4
	v_fma_f32 v84, -v86, v87, 1.0
	v_fmac_f32_e32 v87, v84, v87
	v_div_scale_f32 v84, vcc, 1.0, v85, 1.0
	v_mul_f32_e32 v88, v84, v87
	v_fma_f32 v90, -v86, v88, v84
	v_fmac_f32_e32 v88, v90, v87
	v_fma_f32 v84, -v86, v88, v84
	v_div_fmas_f32 v84, v84, v87, v88
	v_div_fixup_f32 v84, v84, v85, 1.0
	v_mul_f32_e32 v83, v83, v84
	v_mul_f32_e32 v83, v174, v83
	v_bfe_u32 v85, v83, 16, 1
	v_add3_u32 v83, v83, v85, s2
	ds_write_b16_d16_hi v164, v83 offset:6912
	v_mul_f32_e32 v83, v89, v84
	v_mul_f32_e32 v83, v173, v83
	v_bfe_u32 v85, v83, 16, 1
	v_add3_u32 v83, v83, v85, s2
	ds_write_b16_d16_hi v164, v83 offset:6976
	v_mul_f32_e32 v83, v99, v84
	v_mul_f32_e32 v83, v172, v83
	v_bfe_u32 v85, v83, 16, 1
	v_add3_u32 v83, v83, v85, s2
	ds_write_b16_d16_hi v164, v83 offset:7040
	v_mul_f32_e32 v83, v128, v84
	v_mul_f32_e32 v83, v175, v83
	v_bfe_u32 v84, v83, 16, 1
	v_add3_u32 v83, v83, v84, s2
	v_lshlrev_b32_e32 v84, 1, v162
	v_and_b32_e32 v118, 0xf0, v84
	ds_write_b16_d16_hi v164, v83 offset:7104
	v_lshrrev_b32_e32 v83, 4, v163
	v_add_u32_e32 v96, s0, v118
	s_waitcnt lgkmcnt(0)
	v_lshl_add_u32 v84, v83, 8, v96
	v_or_b32_e32 v97, 4, v83
	ds_read_b128 v[84:87], v84
	v_lshl_add_u32 v88, v97, 8, v96
	ds_read_b128 v[88:91], v88
	s_addc_u32 s5, s7, s5
	v_lshl_add_u64 v[92:93], s[4:5], 0, v[118:119]
	v_lshlrev_b32_e32 v118, 11, v83
	v_lshl_add_u64 v[94:95], v[92:93], 0, v[118:119]
	v_lshlrev_b32_e32 v118, 11, v97
	s_waitcnt lgkmcnt(1)
	global_store_dwordx4 v[94:95], v[84:87], off sc1
	v_or_b32_e32 v97, 12, v83
	s_mov_b64 s[4:5], 0
	v_lshl_add_u64 v[84:85], v[92:93], 0, v[118:119]
	s_waitcnt lgkmcnt(0)
	global_store_dwordx4 v[84:85], v[88:91], off sc1
	s_nop 1
	v_or_b32_e32 v88, 8, v83
	v_lshl_add_u32 v84, v88, 8, v96
	ds_read_b128 v[84:87], v84
	v_lshlrev_b32_e32 v118, 11, v88
	v_lshl_add_u32 v88, v97, 8, v96
	ds_read_b128 v[88:91], v88
	v_lshl_add_u64 v[94:95], v[92:93], 0, v[118:119]
	v_lshlrev_b32_e32 v118, 11, v97
	s_waitcnt lgkmcnt(1)
	global_store_dwordx4 v[94:95], v[84:87], off sc1
	v_or_b32_e32 v97, 20, v83
	s_nop 0
	v_lshl_add_u64 v[84:85], v[92:93], 0, v[118:119]
	s_waitcnt lgkmcnt(0)
	global_store_dwordx4 v[84:85], v[88:91], off sc1
	s_nop 1
	v_or_b32_e32 v88, 16, v83
	v_lshl_add_u32 v84, v88, 8, v96
	ds_read_b128 v[84:87], v84
	v_lshlrev_b32_e32 v118, 11, v88
	v_lshl_add_u32 v88, v97, 8, v96
	ds_read_b128 v[88:91], v88
	v_lshl_add_u64 v[94:95], v[92:93], 0, v[118:119]
	v_lshlrev_b32_e32 v118, 11, v97
	s_waitcnt lgkmcnt(1)
	global_store_dwordx4 v[94:95], v[84:87], off sc1
	s_nop 1
	v_lshl_add_u64 v[84:85], v[92:93], 0, v[118:119]
	s_waitcnt lgkmcnt(0)
	global_store_dwordx4 v[84:85], v[88:91], off sc1
	s_nop 1
	v_or_b32_e32 v88, 24, v83
	v_lshl_add_u32 v84, v88, 8, v96
	v_or_b32_e32 v83, 28, v83
	ds_read_b128 v[84:87], v84
	v_lshlrev_b32_e32 v118, 11, v88
	v_lshl_add_u32 v88, v83, 8, v96
	ds_read_b128 v[88:91], v88
	v_lshl_add_u64 v[94:95], v[92:93], 0, v[118:119]
	v_lshlrev_b32_e32 v118, 11, v83
	s_waitcnt lgkmcnt(1)
	global_store_dwordx4 v[94:95], v[84:87], off sc1
	s_nop 1
	v_lshl_add_u64 v[84:85], v[92:93], 0, v[118:119]
	s_waitcnt lgkmcnt(0)
	global_store_dwordx4 v[84:85], v[88:91], off sc1

.LBB0_299:
	s_nop 0
	v_lshl_add_u64 v[4:5], v[18:19], 0, v[14:15]
	v_add_co_u32_e64 v48, s[20:21], s1, v4
	v_add_u32_e32 v7, s37, v105
	s_nop 0
	v_addc_co_u32_e64 v49, s[20:21], 0, v5, s[20:21]
	v_add_u32_e32 v8, s37, v103
	v_add_co_u32_e64 v46, s[20:21], s2, v4
	v_lshl_add_u64 v[2:3], v[20:21], 0, v[14:15]
	v_mov_b32_e32 v6, s37
	s_add_i32 s6, s37, 1
	s_add_i32 s8, s37, 2
	v_add_u32_e32 v9, 1, v7
	v_cmp_lt_i32_e64 s[4:5], s37, v104
	v_add_u32_e32 v51, 1, v8
	v_addc_co_u32_e64 v47, s[20:21], 0, v5, s[20:21]
	v_add_co_u32_e32 v10, vcc, 0x15c00000, v2
	v_add_u32_e32 v12, 2, v7
	v_mov_b32_e32 v13, s6
	v_cmp_lt_i32_e64 s[6:7], s6, v104
	v_add_u32_e32 v23, 3, v7
	v_mov_b32_e32 v25, s8
	v_cmp_lt_i32_e64 s[8:9], s8, v104
	v_add_u32_e32 v52, 2, v8
	v_add_co_u32_e64 v40, s[20:21], s3, v4
	v_cndmask_b32_e64 v6, v9, v6, s[4:5]
	v_cmp_lt_i32_e64 s[4:5], v51, v102
	v_add_u32_e32 v53, 3, v8
	v_add_u32_e32 v54, 4, v8
	v_add_u32_e32 v55, 5, v8
	v_addc_co_u32_e64 v41, s[20:21], 0, v5, s[20:21]
	v_add_u32_e32 v56, 6, v8
	v_add_u32_e32 v57, 7, v8
	v_add_u32_e32 v59, 8, v8
	v_addc_co_u32_e32 v11, vcc, 0, v3, vcc
	v_cndmask_b32_e64 v8, v12, v13, s[6:7]
	v_cndmask_b32_e64 v12, v23, v25, s[8:9]
	v_cndmask_b32_e64 v23, 1.0, 0, s[4:5]
	v_cmp_lt_i32_e64 s[4:5], v52, v102
	v_add_co_u32_e64 v38, s[20:21], s33, v4
	v_add_co_u32_e32 v4, vcc, 0x15c01000, v2
	v_cndmask_b32_e64 v195, 1.0, 0, s[4:5]
	v_cmp_lt_i32_e64 s[4:5], v53, v102
	s_add_i32 s18, s37, 7
	v_addc_co_u32_e64 v39, s[20:21], 0, v5, s[20:21]
	v_cndmask_b32_e64 v197, 1.0, 0, s[4:5]
	v_cmp_lt_i32_e64 s[4:5], v54, v102
	v_addc_co_u32_e32 v5, vcc, 0, v3, vcc
	v_add_u32_e32 v27, 4, v7
	v_add_u32_e32 v31, 5, v7
	v_add_u32_e32 v35, 6, v7
	v_add_u32_e32 v42, 7, v7
	v_add_u32_e32 v7, 8, v7
	v_mov_b32_e32 v50, s18
	v_cmp_lt_i32_e64 s[18:19], s18, v104
	v_cndmask_b32_e64 v199, 1.0, 0, s[4:5]
	v_cmp_lt_i32_e64 s[4:5], v55, v102
	v_add_co_u32_e32 v68, vcc, 0x15c02000, v2
	s_add_i32 s10, s37, 3
	s_add_i32 s12, s37, 4
	s_add_i32 s14, s37, 5
	s_add_i32 s16, s37, 6
	v_cndmask_b32_e64 v66, v7, v50, s[18:19]
	v_min_i32_e32 v25, v51, v102
	v_min_i32_e32 v50, v52, v102
	v_min_i32_e32 v51, v53, v102
	v_min_i32_e32 v52, v54, v102
	v_min_i32_e32 v53, v55, v102
	v_cndmask_b32_e64 v107, 1.0, 0, s[4:5]
	v_min_i32_e32 v54, v56, v102
	v_cmp_lt_i32_e64 s[4:5], v56, v102
	v_min_i32_e32 v55, v57, v102
	v_min_i32_e32 v56, v59, v102
	v_addc_co_u32_e32 v69, vcc, 0, v3, vcc
	v_mov_b32_e32 v29, s10
	v_cmp_lt_i32_e64 s[10:11], s10, v104
	v_mov_b32_e32 v33, s12
	v_cmp_lt_i32_e64 s[12:13], s12, v104
	v_mov_b32_e32 v37, s14
	v_cmp_lt_i32_e64 s[14:15], s14, v104
	v_mov_b32_e32 v44, s16
	v_cmp_lt_i32_e64 s[16:17], s16, v104
	v_cndmask_b32_e64 v106, 1.0, 0, s[4:5]
	v_cmp_lt_i32_e64 s[4:5], v57, v102
	v_cvt_f32_i32_e32 v97, v50
	v_cvt_f32_i32_e32 v98, v51
	v_cvt_f32_i32_e32 v99, v52
	v_cvt_f32_i32_e32 v100, v53
	v_cvt_f32_i32_e32 v101, v54
	v_cvt_f32_i32_e32 v124, v55
	v_cvt_f32_i32_e32 v125, v56
	global_load_dwordx4 v[50:53], v[10:11], off offset:3072
	global_load_dwordx4 v[54:57], v[4:5], off offset:3072
	v_add_co_u32_e32 v4, vcc, 0x15c03000, v2
	v_cndmask_b32_e64 v58, v27, v29, s[10:11]
	v_cndmask_b32_e64 v60, v31, v33, s[12:13]
	v_cndmask_b32_e64 v62, v35, v37, s[14:15]
	v_cndmask_b32_e64 v64, v42, v44, s[16:17]
	v_addc_co_u32_e32 v5, vcc, 0, v3, vcc
	v_cndmask_b32_e64 v44, 1.0, 0, s[4:5]
	v_cmp_lt_i32_e64 s[4:5], v59, v102
	v_ashrrev_i32_e32 v7, 31, v6
	v_ashrrev_i32_e32 v13, 31, v12
	v_ashrrev_i32_e32 v59, 31, v58
	v_ashrrev_i32_e32 v61, 31, v60
	v_ashrrev_i32_e32 v63, 31, v62
	v_ashrrev_i32_e32 v65, 31, v64
	v_ashrrev_i32_e32 v67, 31, v66
	v_add_co_u32_e32 v86, vcc, 0x15c04000, v2
	v_ashrrev_i32_e32 v9, 31, v8
	v_lshlrev_b64 v[6:7], 12, v[6:7]
	v_lshlrev_b64 v[10:11], 12, v[12:13]
	v_lshlrev_b64 v[12:13], 12, v[58:59]
	v_lshlrev_b64 v[58:59], 12, v[60:61]
	v_lshlrev_b64 v[60:61], 12, v[62:63]
	v_lshlrev_b64 v[62:63], 12, v[64:65]
	v_lshlrev_b64 v[64:65], 12, v[66:67]
	v_addc_co_u32_e32 v87, vcc, 0, v3, vcc
	v_lshlrev_b64 v[8:9], 12, v[8:9]
	v_lshl_add_u64 v[6:7], v[16:17], 0, v[6:7]
	v_lshl_add_u64 v[88:89], v[16:17], 0, v[58:59]
	v_lshl_add_u64 v[90:91], v[16:17], 0, v[60:61]
	v_lshl_add_u64 v[92:93], v[16:17], 0, v[62:63]
	v_lshl_add_u64 v[94:95], v[16:17], 0, v[64:65]
	global_load_dwordx4 v[58:61], v[68:69], off offset:3072
	global_load_dwordx4 v[62:65], v[4:5], off offset:3072
	v_add_co_u32_e32 v4, vcc, 0x15c05000, v2
	v_lshl_add_u64 v[8:9], v[16:17], 0, v[8:9]
	v_lshl_add_u64 v[10:11], v[16:17], 0, v[10:11]
	v_lshl_add_u64 v[12:13], v[16:17], 0, v[12:13]
	global_load_dwordx4 v[66:69], v[6:7], off offset:3072
	global_load_dwordx4 v[70:73], v[8:9], off offset:3072
	global_load_dwordx4 v[74:77], v[10:11], off offset:3072
	global_load_dwordx4 v[78:81], v[12:13], off offset:3072
	global_load_dwordx4 v[82:85], v[88:89], off offset:3072
	global_load_dwordx4 v[108:111], v[90:91], off offset:3072
	global_load_dwordx4 v[112:115], v[92:93], off offset:3072
	global_load_dwordx4 v[116:119], v[94:95], off offset:3072
	v_addc_co_u32_e32 v5, vcc, 0, v3, vcc
	v_add_co_u32_e32 v6, vcc, 0x15c06000, v2
	global_load_dwordx4 v[120:123], v[86:87], off offset:3072
	global_load_dwordx4 v[10:13], v[4:5], off offset:3072
	v_addc_co_u32_e32 v7, vcc, 0, v3, vcc
	v_add_co_u32_e32 v2, vcc, 0x15c07000, v2
	v_cvt_f32_i32_e32 v96, v25
	s_nop 0
	v_addc_co_u32_e32 v3, vcc, 0, v3, vcc
	global_load_dwordx4 v[6:9], v[6:7], off offset:3072
	s_nop 0
	global_load_dwordx4 v[2:5], v[2:3], off offset:3072
	v_cndmask_b32_e64 v42, 1.0, 0, s[4:5]
	v_div_scale_f32 v88, s[4:5], v96, v96, 1.0
	v_div_scale_f32 v90, s[6:7], v97, v97, 1.0
	v_rcp_f32_e32 v86, v88
	v_div_scale_f32 v92, s[8:9], v98, v98, 1.0
	v_rcp_f32_e32 v87, v90
	v_div_scale_f32 v94, s[10:11], v99, v99, 1.0
	v_rcp_f32_e32 v134, v92
	v_div_scale_f32 v126, s[12:13], v100, v100, 1.0
	v_rcp_f32_e32 v135, v94
	v_div_scale_f32 v128, s[14:15], v101, v101, 1.0
	v_rcp_f32_e32 v136, v126
	v_fma_f32 v140, -v88, v86, 1.0
	v_div_scale_f32 v89, s[4:5], 1.0, v96, 1.0
	v_div_scale_f32 v130, s[16:17], v124, v124, 1.0
	v_rcp_f32_e32 v137, v128
	v_fma_f32 v141, -v90, v87, 1.0
	v_fmac_f32_e32 v86, v140, v86
	v_div_scale_f32 v91, s[6:7], 1.0, v97, 1.0
	v_div_scale_f32 v132, s[18:19], v125, v125, 1.0
	v_rcp_f32_e32 v138, v130
	v_fma_f32 v142, -v92, v134, 1.0
	v_fmac_f32_e32 v87, v141, v87
	v_mul_f32_e32 v140, v89, v86
	v_div_scale_f32 v93, s[8:9], 1.0, v98, 1.0
	v_rcp_f32_e32 v139, v132
	v_fma_f32 v143, -v94, v135, 1.0
	v_fmac_f32_e32 v134, v142, v134
	v_mul_f32_e32 v141, v91, v87
	v_fma_f32 v148, -v88, v140, v89
	v_div_scale_f32 v95, s[10:11], 1.0, v99, 1.0
	v_fma_f32 v144, -v126, v136, 1.0
	v_fmac_f32_e32 v135, v143, v135
	v_mul_f32_e32 v142, v93, v134
	v_fma_f32 v149, -v90, v141, v91
	v_fmac_f32_e32 v140, v148, v86
	v_div_scale_f32 v127, s[12:13], 1.0, v100, 1.0
	v_fma_f32 v145, -v128, v137, 1.0
	v_fmac_f32_e32 v136, v144, v136
	v_mul_f32_e32 v143, v95, v135
	v_fma_f32 v150, -v92, v142, v93
	v_fmac_f32_e32 v141, v149, v87
	v_fma_f32 v88, -v88, v140, v89
	s_mov_b64 vcc, s[4:5]
	v_div_scale_f32 v129, s[14:15], 1.0, v101, 1.0
	v_fma_f32 v146, -v130, v138, 1.0
	v_fmac_f32_e32 v137, v145, v137
	v_mul_f32_e32 v144, v127, v136
	v_fma_f32 v151, -v94, v143, v95
	v_fmac_f32_e32 v142, v150, v134
	v_fma_f32 v89, -v90, v141, v91
	v_div_fmas_f32 v86, v88, v86, v140
	s_mov_b64 vcc, s[6:7]
	v_div_scale_f32 v131, s[16:17], 1.0, v124, 1.0
	v_fma_f32 v147, -v132, v139, 1.0
	v_fmac_f32_e32 v138, v146, v138
	v_mul_f32_e32 v145, v129, v137
	v_fma_f32 v152, -v126, v144, v127
	v_fmac_f32_e32 v143, v151, v135
	v_fma_f32 v90, -v92, v142, v93
	v_div_fixup_f32 v201, v86, v96, 1.0
	v_div_fmas_f32 v86, v89, v87, v141
	s_mov_b64 vcc, s[8:9]
	v_div_scale_f32 v133, s[18:19], 1.0, v125, 1.0
	v_fmac_f32_e32 v139, v147, v139
	v_mul_f32_e32 v146, v131, v138
	v_fma_f32 v153, -v128, v145, v129
	v_fmac_f32_e32 v144, v152, v136
	v_fma_f32 v91, -v94, v143, v95
	v_div_fixup_f32 v203, v86, v97, 1.0
	v_div_fmas_f32 v86, v90, v134, v142
	s_mov_b64 vcc, s[10:11]
	v_mul_f32_e32 v147, v133, v139
	v_fma_f32 v154, -v130, v146, v131
	v_fmac_f32_e32 v145, v153, v137
	v_fma_f32 v92, -v126, v144, v127
	v_div_fixup_f32 v205, v86, v98, 1.0
	v_div_fmas_f32 v86, v91, v135, v143
	s_mov_b64 vcc, s[12:13]
	v_fma_f32 v155, -v132, v147, v133
	v_fmac_f32_e32 v146, v154, v138
	v_fma_f32 v93, -v128, v145, v129
	v_div_fixup_f32 v207, v86, v99, 1.0
	v_div_fmas_f32 v86, v92, v136, v144
	s_mov_b64 vcc, s[14:15]
	v_fmac_f32_e32 v147, v155, v139
	v_fma_f32 v94, -v130, v146, v131
	v_div_fixup_f32 v209, v86, v100, 1.0
	v_div_fmas_f32 v86, v93, v137, v145
	s_mov_b64 vcc, s[16:17]
	v_fma_f32 v95, -v132, v147, v133
	v_div_fixup_f32 v211, v86, v101, 1.0
	v_div_fmas_f32 v86, v94, v138, v146
	s_mov_b64 vcc, s[18:19]
	v_mov_b32_e32 v31, v23
	v_mov_b32_e32 v25, v23
	v_mov_b32_e32 v27, v23
	v_mov_b32_e32 v35, v23
	v_mov_b32_e32 v29, v23
	v_mov_b32_e32 v37, v23
	v_div_fixup_f32 v213, v86, v124, 1.0
	v_div_fmas_f32 v86, v95, v139, v147
	s_waitcnt vmcnt(15)
	v_and_b32_e32 v126, 0xffff0000, v50
	v_lshlrev_b32_e32 v128, 16, v51
	v_lshlrev_b32_e32 v132, 16, v52
	v_and_b32_e32 v134, 0xffff0000, v52
	v_lshlrev_b32_e32 v136, 16, v53
	v_and_b32_e32 v138, 0xffff0000, v53
	s_waitcnt vmcnt(11)
	v_and_b32_e32 v127, 0xffff0000, v66
	v_lshlrev_b32_e32 v129, 16, v67
	v_lshlrev_b32_e32 v133, 16, v68
	v_and_b32_e32 v135, 0xffff0000, v68
	v_lshlrev_b32_e32 v137, 16, v69
	v_and_b32_e32 v139, 0xffff0000, v69
	v_mov_b32_e32 v33, v23
	v_div_fixup_f32 v215, v86, v125, 1.0
	v_lshlrev_b32_e32 v124, 16, v50
	v_and_b32_e32 v130, 0xffff0000, v51
	v_lshlrev_b32_e32 v125, 16, v66
	v_and_b32_e32 v131, 0xffff0000, v67
	s_waitcnt vmcnt(10)
	v_lshlrev_b32_e32 v141, 16, v70
	v_and_b32_e32 v143, 0xffff0000, v70
	v_lshlrev_b32_e32 v145, 16, v71
	v_and_b32_e32 v147, 0xffff0000, v71
	v_lshlrev_b32_e32 v149, 16, v72
	v_and_b32_e32 v151, 0xffff0000, v72
	v_lshlrev_b32_e32 v153, 16, v73
	v_and_b32_e32 v155, 0xffff0000, v73
	s_waitcnt vmcnt(9)
	v_lshlrev_b32_e32 v157, 16, v74
	v_and_b32_e32 v159, 0xffff0000, v74
	v_lshlrev_b32_e32 v161, 16, v75
	v_and_b32_e32 v163, 0xffff0000, v75
	s_waitcnt vmcnt(6)
	v_and_b32_e32 v71, 0xffff0000, v108
	v_and_b32_e32 v73, 0xffff0000, v109
	v_and_b32_e32 v75, 0xffff0000, v110
	s_waitcnt vmcnt(5)
	v_lshlrev_b32_e32 v69, 16, v115
	s_waitcnt vmcnt(4)
	v_lshlrev_b32_e32 v53, 16, v119
	v_and_b32_e32 v51, 0xffff0000, v119
	v_pk_add_f32 v[30:31], v[30:31], v[126:127]
	v_pk_add_f32 v[24:25], v[24:25], v[128:129]
	v_pk_add_f32 v[26:27], v[26:27], v[132:133]
	v_pk_add_f32 v[34:35], v[34:35], v[134:135]
	v_pk_add_f32 v[28:29], v[28:29], v[136:137]
	v_pk_add_f32 v[36:37], v[36:37], v[138:139]
	v_mul_f32_e32 v50, v23, v127
	v_mul_f32_e32 v52, v23, v129
	v_mul_f32_e32 v68, v23, v133
	v_mul_f32_e32 v70, v23, v135
	v_mul_f32_e32 v72, v23, v137
	v_mul_f32_e32 v74, v23, v139
	v_lshlrev_b32_e32 v172, 16, v62
	v_and_b32_e32 v174, 0xffff0000, v62
	v_lshlrev_b32_e32 v176, 16, v63
	v_and_b32_e32 v178, 0xffff0000, v63
	v_lshlrev_b32_e32 v180, 16, v64
	v_and_b32_e32 v182, 0xffff0000, v64
	v_lshlrev_b32_e32 v184, 16, v65
	v_and_b32_e32 v186, 0xffff0000, v65
	v_lshlrev_b32_e32 v99, 16, v83
	v_and_b32_e32 v89, 0xffff0000, v83
	v_lshlrev_b32_e32 v95, 16, v85
	v_and_b32_e32 v93, 0xffff0000, v85
	v_lshlrev_b32_e32 v85, 16, v108
	v_lshlrev_b32_e32 v83, 16, v109
	v_and_b32_e32 v65, 0xffff0000, v115
	v_lshlrev_b32_e32 v62, 16, v113
	v_and_b32_e32 v63, 0xffff0000, v113
	v_pk_add_f32 v[108:109], v[22:23], v[124:125]
	v_pk_add_f32 v[32:33], v[32:33], v[130:131]
	v_mul_f32_e32 v22, v23, v125
	v_mul_f32_e32 v64, v23, v131
	s_waitcnt vmcnt(3)
	v_lshlrev_b32_e32 v98, 16, v121
	v_and_b32_e32 v88, 0xffff0000, v121
	v_lshlrev_b32_e32 v94, 16, v123
	v_and_b32_e32 v92, 0xffff0000, v123
	v_fma_f32 v113, v201, v30, -v126
	v_fma_f32 v115, v201, v24, -v128
	v_fma_f32 v119, v201, v26, -v132
	v_fma_f32 v121, v201, v34, -v134
	v_fma_f32 v123, v201, v28, -v136
	v_fma_f32 v125, v201, v36, -v138
	v_pk_add_f32 v[30:31], v[30:31], v[50:51] op_sel_hi:[1,0] neg_lo:[0,1] neg_hi:[0,1]
	v_pk_add_f32 v[24:25], v[24:25], v[52:53] op_sel_hi:[1,0] neg_lo:[0,1] neg_hi:[0,1]
	v_pk_add_f32 v[26:27], v[26:27], v[68:69] op_sel_hi:[1,0] neg_lo:[0,1] neg_hi:[0,1]
	v_pk_add_f32 v[34:35], v[34:35], v[70:71] op_sel_hi:[1,0] neg_lo:[0,1] neg_hi:[0,1]
	v_pk_add_f32 v[28:29], v[28:29], v[72:73] op_sel_hi:[1,0] neg_lo:[0,1] neg_hi:[0,1]
	v_pk_add_f32 v[36:37], v[36:37], v[74:75] op_sel_hi:[1,0] neg_lo:[0,1] neg_hi:[0,1]
	v_and_b32_e32 v142, 0xffff0000, v54
	v_lshlrev_b32_e32 v144, 16, v55
	v_lshlrev_b32_e32 v148, 16, v56
	v_and_b32_e32 v150, 0xffff0000, v56
	v_lshlrev_b32_e32 v152, 16, v57
	v_and_b32_e32 v154, 0xffff0000, v57
	v_lshlrev_b32_e32 v156, 16, v58
	v_and_b32_e32 v158, 0xffff0000, v58
	v_lshlrev_b32_e32 v160, 16, v59
	v_and_b32_e32 v162, 0xffff0000, v59
	v_lshlrev_b32_e32 v165, 16, v76
	v_and_b32_e32 v167, 0xffff0000, v76
	v_lshlrev_b32_e32 v169, 16, v77
	v_and_b32_e32 v171, 0xffff0000, v77
	v_lshlrev_b32_e32 v173, 16, v78
	v_and_b32_e32 v175, 0xffff0000, v78
	v_lshlrev_b32_e32 v177, 16, v79
	v_and_b32_e32 v179, 0xffff0000, v79
	v_lshlrev_b32_e32 v181, 16, v80
	v_and_b32_e32 v183, 0xffff0000, v80
	v_lshlrev_b32_e32 v101, 16, v82
	v_and_b32_e32 v87, 0xffff0000, v82
	v_lshlrev_b32_e32 v97, 16, v84
	v_and_b32_e32 v91, 0xffff0000, v84
	v_lshlrev_b32_e32 v79, 16, v111
	v_and_b32_e32 v77, 0xffff0000, v111
	v_lshlrev_b32_e32 v58, 16, v117
	v_and_b32_e32 v59, 0xffff0000, v117
	v_fma_f32 v111, v201, v108, -v124
	v_fma_f32 v117, v201, v32, -v130
	v_pk_add_f32 v[22:23], v[108:109], v[22:23] op_sel_hi:[1,0] neg_lo:[0,1] neg_hi:[0,1]
	v_pk_add_f32 v[32:33], v[32:33], v[64:65] op_sel_hi:[1,0] neg_lo:[0,1] neg_hi:[0,1]
	s_waitcnt vmcnt(2)
	v_lshlrev_b32_e32 v84, 16, v10
	v_and_b32_e32 v70, 0xffff0000, v10
	v_lshlrev_b32_e32 v82, 16, v11
	v_and_b32_e32 v72, 0xffff0000, v11
	v_lshlrev_b32_e32 v80, 16, v12
	v_and_b32_e32 v74, 0xffff0000, v12
	v_lshlrev_b32_e32 v78, 16, v13
	v_and_b32_e32 v76, 0xffff0000, v13
	v_cvt_pk_bf16_f32 v10, v111, v113
	v_cvt_pk_bf16_f32 v11, v115, v117
	v_cvt_pk_bf16_f32 v12, v119, v121
	v_cvt_pk_bf16_f32 v13, v123, v125
	v_mov_b32_e32 v31, v195
	v_mov_b32_e32 v25, v195
	v_mov_b32_e32 v27, v195
	v_mov_b32_e32 v35, v195
	v_mov_b32_e32 v29, v195
	v_mov_b32_e32 v37, v195
	v_lshlrev_b32_e32 v140, 16, v54
	v_and_b32_e32 v146, 0xffff0000, v55
	v_mov_b32_e32 v23, v195
	v_mov_b32_e32 v33, v195
	global_store_dwordx4 v[48:49], v[10:13], off offset:1024 sc1
	v_pk_add_f32 v[28:29], v[28:29], v[152:153]
	v_lshlrev_b32_e32 v164, 16, v60
	v_pk_add_f32 v[10:11], v[30:31], v[142:143]
	v_pk_add_f32 v[12:13], v[24:25], v[144:145]
	v_pk_add_f32 v[24:25], v[26:27], v[148:149]
	v_pk_add_f32 v[26:27], v[34:35], v[150:151]
	v_pk_add_f32 v[30:31], v[36:37], v[154:155]
	v_and_b32_e32 v166, 0xffff0000, v60
	v_lshlrev_b32_e32 v168, 16, v61
	v_and_b32_e32 v170, 0xffff0000, v61
	v_lshlrev_b32_e32 v185, 16, v81
	v_and_b32_e32 v187, 0xffff0000, v81
	v_lshlrev_b32_e32 v81, 16, v110
	v_lshlrev_b32_e32 v60, 16, v112
	v_and_b32_e32 v61, 0xffff0000, v112
	v_lshlrev_b32_e32 v54, 16, v116
	v_and_b32_e32 v55, 0xffff0000, v116
	v_lshlrev_b32_e32 v66, 16, v114
	v_and_b32_e32 v67, 0xffff0000, v114
	v_lshlrev_b32_e32 v56, 16, v118
	v_and_b32_e32 v57, 0xffff0000, v118
	v_mul_f32_e32 v110, v195, v141
	v_mul_f32_e32 v112, v195, v143
	v_mul_f32_e32 v114, v195, v145
	v_mul_f32_e32 v116, v195, v147
	v_mul_f32_e32 v118, v195, v149
	v_mul_f32_e32 v196, v195, v151
	v_mul_f32_e32 v198, v195, v153
	v_mul_f32_e32 v200, v195, v155
	s_waitcnt vmcnt(2)
	v_lshlrev_b32_e32 v68, 16, v9
	v_and_b32_e32 v64, 0xffff0000, v9
	v_lshlrev_b32_e32 v238, 16, v8
	v_and_b32_e32 v239, 0xffff0000, v8
	v_pk_add_f32 v[8:9], v[22:23], v[140:141]
	v_pk_add_f32 v[22:23], v[32:33], v[146:147]
	v_fma_f32 v111, v203, v26, -v150
	v_fma_f32 v113, v203, v28, -v152
	v_fma_f32 v115, v203, v30, -v154
	s_waitcnt vmcnt(1)
	v_lshlrev_b32_e32 v32, 16, v2
	v_and_b32_e32 v33, 0xffff0000, v2
	v_lshlrev_b32_e32 v34, 16, v3
	v_and_b32_e32 v35, 0xffff0000, v3
	v_lshlrev_b32_e32 v36, 16, v4
	v_and_b32_e32 v37, 0xffff0000, v4
	v_lshlrev_b32_e32 v52, 16, v5
	v_and_b32_e32 v50, 0xffff0000, v5
	v_fma_f32 v2, v203, v8, -v140
	v_fma_f32 v3, v203, v10, -v142
	v_fma_f32 v4, v203, v12, -v144
	v_fma_f32 v5, v203, v22, -v146
	v_fma_f32 v109, v203, v24, -v148
	v_pk_add_f32 v[8:9], v[8:9], v[110:111] op_sel_hi:[1,0] neg_lo:[0,1] neg_hi:[0,1]
	v_pk_add_f32 v[10:11], v[10:11], v[112:113] op_sel_hi:[1,0] neg_lo:[0,1] neg_hi:[0,1]
	v_pk_add_f32 v[12:13], v[12:13], v[114:115] op_sel_hi:[1,0] neg_lo:[0,1] neg_hi:[0,1]
	v_pk_add_f32 v[22:23], v[22:23], v[116:117] op_sel_hi:[1,0] neg_lo:[0,1] neg_hi:[0,1]
	v_pk_add_f32 v[24:25], v[24:25], v[118:119] op_sel_hi:[1,0] neg_lo:[0,1] neg_hi:[0,1]
	v_pk_add_f32 v[26:27], v[26:27], v[196:197] op_sel_hi:[1,0] neg_lo:[0,1] neg_hi:[0,1]
	v_pk_add_f32 v[28:29], v[28:29], v[198:199] op_sel_hi:[1,0] neg_lo:[0,1] neg_hi:[0,1]
	v_pk_add_f32 v[30:31], v[30:31], v[200:201] op_sel_hi:[1,0] neg_lo:[0,1] neg_hi:[0,1]
	v_cvt_pk_bf16_f32 v2, v2, v3
	v_cvt_pk_bf16_f32 v3, v4, v5
	v_cvt_pk_bf16_f32 v4, v109, v111
	v_cvt_pk_bf16_f32 v5, v113, v115
	v_mov_b32_e32 v9, v197
	v_mov_b32_e32 v11, v197
	v_mov_b32_e32 v13, v197
	v_mov_b32_e32 v23, v197
	v_mov_b32_e32 v25, v197
	v_mov_b32_e32 v27, v197
	v_mov_b32_e32 v29, v197
	v_mov_b32_e32 v31, v197
	v_mul_f32_e32 v202, v197, v157
	v_mul_f32_e32 v204, v197, v159
	v_mul_f32_e32 v206, v197, v161
	v_mul_f32_e32 v208, v197, v163
	v_mul_f32_e32 v210, v197, v165
	v_mul_f32_e32 v212, v197, v167
	v_mul_f32_e32 v214, v197, v169
	v_mul_f32_e32 v216, v197, v171
	global_store_dwordx4 v[48:49], v[2:5], off offset:3072 sc1
	v_lshlrev_b32_e32 v100, 16, v120
	v_mul_f32_e32 v218, v199, v173
	v_pk_add_f32 v[2:3], v[8:9], v[156:157]
	v_pk_add_f32 v[4:5], v[10:11], v[158:159]
	v_pk_add_f32 v[8:9], v[12:13], v[160:161]
	v_pk_add_f32 v[10:11], v[22:23], v[162:163]
	v_pk_add_f32 v[12:13], v[24:25], v[164:165]
	v_pk_add_f32 v[22:23], v[26:27], v[166:167]
	v_pk_add_f32 v[24:25], v[28:29], v[168:169]
	v_pk_add_f32 v[26:27], v[30:31], v[170:171]
	v_fma_f32 v109, v205, v8, -v160
	v_fma_f32 v110, v205, v10, -v162
	v_fma_f32 v111, v205, v12, -v164
	v_fma_f32 v112, v205, v22, -v166
	v_fma_f32 v113, v205, v24, -v168
	v_fma_f32 v114, v205, v26, -v170
	v_pk_add_f32 v[28:29], v[2:3], v[202:203] op_sel_hi:[1,0] neg_lo:[0,1] neg_hi:[0,1]
	v_pk_add_f32 v[30:31], v[4:5], v[204:205] op_sel_hi:[1,0] neg_lo:[0,1] neg_hi:[0,1]
	v_pk_add_f32 v[8:9], v[8:9], v[206:207] op_sel_hi:[1,0] neg_lo:[0,1] neg_hi:[0,1]
	v_pk_add_f32 v[10:11], v[10:11], v[208:209] op_sel_hi:[1,0] neg_lo:[0,1] neg_hi:[0,1]
	v_pk_add_f32 v[12:13], v[12:13], v[210:211] op_sel_hi:[1,0] neg_lo:[0,1] neg_hi:[0,1]
	v_pk_add_f32 v[22:23], v[22:23], v[212:213] op_sel_hi:[1,0] neg_lo:[0,1] neg_hi:[0,1]
	v_pk_add_f32 v[24:25], v[24:25], v[214:215] op_sel_hi:[1,0] neg_lo:[0,1] neg_hi:[0,1]
	v_pk_add_f32 v[26:27], v[26:27], v[216:217] op_sel_hi:[1,0] neg_lo:[0,1] neg_hi:[0,1]
	v_fma_f32 v48, v205, v2, -v156
	v_fma_f32 v49, v205, v4, -v158
	v_cvt_pk_bf16_f32 v2, v48, v49
	v_cvt_pk_bf16_f32 v3, v109, v110
	v_cvt_pk_bf16_f32 v4, v111, v112
	v_cvt_pk_bf16_f32 v5, v113, v114
	v_mov_b32_e32 v29, v199
	v_mov_b32_e32 v31, v199
	v_mov_b32_e32 v9, v199
	v_mov_b32_e32 v11, v199
	v_mov_b32_e32 v13, v199
	v_mov_b32_e32 v23, v199
	v_mov_b32_e32 v25, v199
	v_mov_b32_e32 v27, v199
	v_and_b32_e32 v86, 0xffff0000, v120
	v_mul_f32_e32 v120, v199, v175
	v_mul_f32_e32 v220, v199, v177
	v_mul_f32_e32 v222, v199, v179
	v_lshlrev_b32_e32 v96, 16, v122
	v_mul_f32_e32 v224, v199, v181
	v_and_b32_e32 v90, 0xffff0000, v122
	v_mul_f32_e32 v122, v199, v183
	v_mul_f32_e32 v226, v199, v185
	v_mul_f32_e32 v228, v199, v187
	global_store_dwordx4 v[46:47], v[2:5], off offset:1024 sc1
	v_pk_add_f32 v[8:9], v[8:9], v[176:177]
	v_pk_add_f32 v[10:11], v[10:11], v[178:179]
	v_pk_add_f32 v[2:3], v[28:29], v[172:173]
	v_pk_add_f32 v[4:5], v[30:31], v[174:175]
	v_pk_add_f32 v[12:13], v[12:13], v[180:181]
	v_pk_add_f32 v[22:23], v[22:23], v[182:183]
	v_pk_add_f32 v[24:25], v[24:25], v[184:185]
	v_pk_add_f32 v[26:27], v[26:27], v[186:187]
	v_fma_f32 v109, v207, v8, -v176
	v_fma_f32 v110, v207, v10, -v178
	v_fma_f32 v111, v207, v12, -v180
	v_fma_f32 v112, v207, v22, -v182
	v_fma_f32 v113, v207, v24, -v184
	v_fma_f32 v114, v207, v26, -v186
	v_pk_add_f32 v[28:29], v[2:3], v[218:219] op_sel_hi:[1,0] neg_lo:[0,1] neg_hi:[0,1]
	v_pk_add_f32 v[30:31], v[4:5], v[120:121] op_sel_hi:[1,0] neg_lo:[0,1] neg_hi:[0,1]
	v_pk_add_f32 v[8:9], v[8:9], v[220:221] op_sel_hi:[1,0] neg_lo:[0,1] neg_hi:[0,1]
	v_pk_add_f32 v[10:11], v[10:11], v[222:223] op_sel_hi:[1,0] neg_lo:[0,1] neg_hi:[0,1]
	v_pk_add_f32 v[12:13], v[12:13], v[224:225] op_sel_hi:[1,0] neg_lo:[0,1] neg_hi:[0,1]
	v_pk_add_f32 v[22:23], v[22:23], v[122:123] op_sel_hi:[1,0] neg_lo:[0,1] neg_hi:[0,1]
	v_pk_add_f32 v[24:25], v[24:25], v[226:227] op_sel_hi:[1,0] neg_lo:[0,1] neg_hi:[0,1]
	v_pk_add_f32 v[26:27], v[26:27], v[228:229] op_sel_hi:[1,0] neg_lo:[0,1] neg_hi:[0,1]
	v_fma_f32 v48, v207, v2, -v172
	v_fma_f32 v49, v207, v4, -v174
	v_cvt_pk_bf16_f32 v2, v48, v49
	v_cvt_pk_bf16_f32 v3, v109, v110
	v_cvt_pk_bf16_f32 v4, v111, v112
	v_cvt_pk_bf16_f32 v5, v113, v114
	v_mov_b32_e32 v29, v107
	v_mov_b32_e32 v31, v107
	v_mov_b32_e32 v9, v107
	v_mov_b32_e32 v11, v107
	v_mov_b32_e32 v13, v107
	v_mov_b32_e32 v23, v107
	v_mov_b32_e32 v25, v107
	v_mov_b32_e32 v27, v107
	v_mul_f32_e32 v230, v107, v101
	v_mul_f32_e32 v232, v107, v87
	v_mul_f32_e32 v234, v107, v99
	v_mul_f32_e32 v124, v107, v89
	v_mul_f32_e32 v126, v107, v97
	v_mul_f32_e32 v128, v107, v91
	v_mul_f32_e32 v130, v107, v95
	v_mul_f32_e32 v132, v107, v93
	global_store_dwordx4 v[46:47], v[2:5], off offset:3072 sc1
	v_pk_add_f32 v[8:9], v[8:9], v[98:99]
	v_pk_add_f32 v[10:11], v[10:11], v[88:89]
	v_pk_add_f32 v[2:3], v[28:29], v[100:101]
	v_pk_add_f32 v[4:5], v[30:31], v[86:87]
	v_pk_add_f32 v[12:13], v[12:13], v[96:97]
	v_pk_add_f32 v[22:23], v[22:23], v[90:91]
	v_pk_add_f32 v[24:25], v[24:25], v[94:95]
	v_pk_add_f32 v[26:27], v[26:27], v[92:93]
	v_fma_f32 v47, v209, v4, -v86
	v_fma_f32 v48, v209, v8, -v98
	v_fma_f32 v49, v209, v10, -v88
	v_fma_f32 v86, v209, v12, -v96
	v_fma_f32 v87, v209, v22, -v90
	v_fma_f32 v88, v209, v24, -v94
	v_fma_f32 v89, v209, v26, -v92
	v_pk_add_f32 v[28:29], v[2:3], v[230:231] op_sel_hi:[1,0] neg_lo:[0,1] neg_hi:[0,1]
	v_pk_add_f32 v[30:31], v[4:5], v[232:233] op_sel_hi:[1,0] neg_lo:[0,1] neg_hi:[0,1]
	v_pk_add_f32 v[8:9], v[8:9], v[234:235] op_sel_hi:[1,0] neg_lo:[0,1] neg_hi:[0,1]
	v_pk_add_f32 v[10:11], v[10:11], v[124:125] op_sel_hi:[1,0] neg_lo:[0,1] neg_hi:[0,1]
	v_pk_add_f32 v[12:13], v[12:13], v[126:127] op_sel_hi:[1,0] neg_lo:[0,1] neg_hi:[0,1]
	v_pk_add_f32 v[22:23], v[22:23], v[128:129] op_sel_hi:[1,0] neg_lo:[0,1] neg_hi:[0,1]
	v_pk_add_f32 v[24:25], v[24:25], v[130:131] op_sel_hi:[1,0] neg_lo:[0,1] neg_hi:[0,1]
	v_pk_add_f32 v[26:27], v[26:27], v[132:133] op_sel_hi:[1,0] neg_lo:[0,1] neg_hi:[0,1]
	v_fma_f32 v46, v209, v2, -v100
	v_cvt_pk_bf16_f32 v2, v46, v47
	v_cvt_pk_bf16_f32 v3, v48, v49
	v_cvt_pk_bf16_f32 v4, v86, v87
	v_cvt_pk_bf16_f32 v5, v88, v89
	v_mov_b32_e32 v29, v106
	v_mov_b32_e32 v31, v106
	v_mov_b32_e32 v9, v106
	v_mov_b32_e32 v11, v106
	v_mov_b32_e32 v13, v106
	v_mov_b32_e32 v23, v106
	v_mov_b32_e32 v25, v106
	v_mov_b32_e32 v27, v106
	v_mul_f32_e32 v108, v106, v79
	v_mul_f32_e32 v134, v106, v77
	global_store_dwordx4 v[40:41], v[2:5], off offset:1024 sc1
	v_pk_add_f32 v[46:47], v[28:29], v[84:85]
	v_pk_add_f32 v[48:49], v[10:11], v[72:73]
	v_pk_mul_f32 v[2:3], v[28:29], v[84:85]
	v_pk_add_f32 v[4:5], v[30:31], v[70:71]
	v_pk_mul_f32 v[28:29], v[30:31], v[70:71]
	v_pk_add_f32 v[30:31], v[8:9], v[82:83]
	v_pk_mul_f32 v[8:9], v[8:9], v[82:83]
	v_pk_mul_f32 v[10:11], v[10:11], v[72:73]
	v_pk_add_f32 v[86:87], v[12:13], v[80:81]
	v_pk_mul_f32 v[12:13], v[12:13], v[80:81]
	v_pk_add_f32 v[88:89], v[22:23], v[74:75]
	v_pk_mul_f32 v[22:23], v[22:23], v[74:75]
	v_pk_add_f32 v[24:25], v[24:25], v[78:79]
	v_pk_add_f32 v[26:27], v[26:27], v[76:77]
	v_fma_f32 v2, v211, v46, -v84
	v_fma_f32 v5, v211, v4, -v70
	v_fma_f32 v8, v211, v30, -v82
	v_fma_f32 v12, v211, v48, -v72
	v_fma_f32 v71, v211, v24, -v78
	v_fma_f32 v72, v211, v26, -v76
	v_pk_add_f32 v[24:25], v[24:25], v[108:109] op_sel_hi:[1,0] neg_lo:[0,1] neg_hi:[0,1]
	v_pk_add_f32 v[26:27], v[26:27], v[134:135] op_sel_hi:[1,0] neg_lo:[0,1] neg_hi:[0,1]
	v_mov_b32_e32 v47, v4
	v_mov_b32_e32 v28, v3
	v_mov_b32_e32 v31, v48
	v_mov_b32_e32 v10, v9
	v_mov_b32_e32 v87, v88
	v_mov_b32_e32 v22, v13
	v_lshlrev_b32_e32 v236, 16, v6
	v_and_b32_e32 v237, 0xffff0000, v6
	v_lshlrev_b32_e32 v6, 16, v7
	v_and_b32_e32 v7, 0xffff0000, v7
	v_fma_f32 v49, v211, v86, -v80
	v_fma_f32 v70, v211, v88, -v74
	v_cvt_pk_bf16_f32 v2, v2, v5
	v_cvt_pk_bf16_f32 v3, v8, v12
	v_cvt_pk_bf16_f32 v4, v49, v70
	v_cvt_pk_bf16_f32 v5, v71, v72
	v_mov_b32_e32 v25, v44
	v_mov_b32_e32 v27, v44
	v_pk_add_f32 v[8:9], v[46:47], v[28:29] neg_lo:[0,1] neg_hi:[0,1]
	v_pk_add_f32 v[10:11], v[30:31], v[10:11] neg_lo:[0,1] neg_hi:[0,1]
	v_pk_add_f32 v[12:13], v[86:87], v[22:23] neg_lo:[0,1] neg_hi:[0,1]
	v_mul_f32_e32 v136, v44, v69
	v_mul_f32_e32 v138, v44, v65
	global_store_dwordx4 v[40:41], v[2:5], off offset:3072 sc1
	v_pk_add_f32 v[8:9], v[8:9], v[236:237]
	v_pk_add_f32 v[10:11], v[10:11], v[6:7]
	v_pk_add_f32 v[2:3], v[24:25], v[68:69]
	v_pk_add_f32 v[4:5], v[26:27], v[64:65]
	v_pk_add_f32 v[12:13], v[12:13], v[238:239]
	v_fma_f32 v24, v213, v8, -v236
	v_fma_f32 v25, v213, v9, -v237
	v_pk_fma_f32 v[8:9], v[44:45], v[60:61], v[8:9] op_sel_hi:[0,1,1] neg_lo:[1,0,0] neg_hi:[1,0,0]
	v_fma_f32 v26, v213, v10, -v6
	v_fma_f32 v27, v213, v11, -v7
	v_pk_fma_f32 v[6:7], v[44:45], v[62:63], v[10:11] op_sel_hi:[0,1,1] neg_lo:[1,0,0] neg_hi:[1,0,0]
	v_fma_f32 v30, v213, v12, -v238
	v_fma_f32 v31, v213, v13, -v239
	v_pk_fma_f32 v[10:11], v[44:45], v[66:67], v[12:13] op_sel_hi:[0,1,1] neg_lo:[1,0,0] neg_hi:[1,0,0]
	v_pk_add_f32 v[12:13], v[2:3], v[136:137] op_sel_hi:[1,0] neg_lo:[0,1] neg_hi:[0,1]
	v_pk_add_f32 v[28:29], v[4:5], v[138:139] op_sel_hi:[1,0] neg_lo:[0,1] neg_hi:[0,1]
	v_fma_f32 v22, v213, v2, -v68
	v_fma_f32 v23, v213, v4, -v64
	v_cvt_pk_bf16_f32 v2, v24, v25
	v_pk_add_f32 v[8:9], v[8:9], v[32:33]
	v_pk_add_f32 v[6:7], v[6:7], v[34:35]
	v_cvt_pk_bf16_f32 v3, v26, v27
	v_pk_add_f32 v[10:11], v[10:11], v[36:37]
	v_cvt_pk_bf16_f32 v4, v30, v31
	v_cvt_pk_bf16_f32 v5, v22, v23
	v_mov_b32_e32 v13, v42
	v_mov_b32_e32 v29, v42
	v_fma_f32 v30, v215, v8, -v32
	v_fma_f32 v31, v215, v9, -v33
	v_pk_fma_f32 v[22:23], v[42:43], v[54:55], v[8:9] op_sel_hi:[0,1,1] neg_lo:[1,0,0] neg_hi:[1,0,0]
	v_fma_f32 v32, v215, v6, -v34
	v_fma_f32 v33, v215, v7, -v35
	v_pk_fma_f32 v[24:25], v[42:43], v[58:59], v[6:7] op_sel_hi:[0,1,1] neg_lo:[1,0,0] neg_hi:[1,0,0]
	v_fma_f32 v34, v215, v10, -v36
	v_fma_f32 v35, v215, v11, -v37
	global_store_dwordx4 v[38:39], v[2:5], off offset:1024 sc1
	v_pk_fma_f32 v[26:27], v[42:43], v[56:57], v[10:11] op_sel_hi:[0,1,1] neg_lo:[1,0,0] neg_hi:[1,0,0]
	v_pk_add_f32 v[6:7], v[12:13], v[52:53]
	v_pk_mul_f32 v[4:5], v[12:13], v[52:53]
	v_pk_add_f32 v[8:9], v[28:29], v[50:51]
	v_pk_mul_f32 v[10:11], v[28:29], v[50:51]
	v_mov_b32_e32 v7, v8
	v_mov_b32_e32 v10, v5
	s_add_i32 s38, s37, 8
	v_pk_add_f32 v[28:29], v[6:7], v[10:11] neg_lo:[0,1] neg_hi:[0,1]
	v_lshl_add_u64 v[18:19], v[18:19], 0, s[30:31]
	v_lshl_add_u64 v[20:21], v[20:21], 0, s[34:35]
	s_cmp_gt_u32 s37, 23
	s_mov_b32 s37, s38
	v_cvt_pk_bf16_f32 v2, v30, v31
	v_cvt_pk_bf16_f32 v3, v32, v33
	v_cvt_pk_bf16_f32 v4, v34, v35
	v_mov_b32_e32 v30, v23
	v_mov_b32_e32 v32, v25
	v_mov_b32_e32 v34, v27
	v_mov_b32_e32 v36, v29
	v_fma_f32 v9, v215, v6, -v52
	v_fma_f32 v12, v215, v8, -v50
	v_cvt_pk_bf16_f32 v5, v9, v12
	global_store_dwordx4 v[38:39], v[2:5], off offset:3072 sc1
	s_cbranch_scc0 .LBB0_299
	v_add_u32_e32 v43, s86, v43
	v_cmp_lt_i32_e32 vcc, s36, v43
	s_or_b64 s[26:27], vcc, s[26:27]
	v_add_u32_e32 v45, s0, v45
	s_andn2_b64 exec, exec, s[26:27]
	s_cbranch_execnz .LBB0_294
